# attention: per-tile barrier and the next tile's LDS-DMA issue moved into the last PV MFMA block (first DMAs issued once before the loop); trip boundary has no barrier
# speedup vs baseline: 1.0092x; 1.0060x over previous
.LBB0_756:
	s_and_b32 s8, s8, 7
	s_ashr_i32 s31, s30, 31
	s_mul_i32 s7, s30, 0xc00
	s_mul_hi_i32 s6, s30, 0xc00
	s_add_u32 s7, s37, s7
	s_addc_u32 s6, s38, s6
	s_mul_i32 s9, s8, 0x180
	s_add_u32 s10, s7, s9
	s_addc_u32 s11, s6, 0
	s_add_u32 s6, s39, s9
	s_addc_u32 s7, s40, 0
	s_lshl_b32 s61, s8, 7
	s_lshl_b32 s8, s8, 8
	s_add_u32 s34, s41, s8
	v_readfirstlane_b32 s9, v254
	s_addc_u32 s35, s42, 0
	s_ashr_i32 s8, s9, 6
	s_lshl_b32 s82, s8, 10
	s_mov_b32 s72, s6
	s_and_b32 s73, s7, 0xffff
	s_mov_b32 s74, 0x7ffffff0
	s_mov_b32 s75, 0x20000
	s_mov_b32 s76, s34
	s_and_b32 s77, s35, 0xffff
	s_mov_b32 s78, 0x7ffffff0
	s_mov_b32 s79, 0x20000
	v_lshl_or_b32 v2, s8, 5, v188
	v_mov_b64_e32 v[0:1], s[10:11]
	v_mad_i64_i32 v[0:1], s[10:11], v2, s46, v[0:1]
	v_lshl_add_u64 v[26:27], s[26:27], 0, v[142:143]
	v_lshl_add_u64 v[28:29], v[146:147], 0, s[26:27]
	v_lshl_add_u64 v[38:39], v[0:1], 0, v[148:149]
	v_lshlrev_b64 v[0:1], 11, v[26:27]
	v_lshlrev_b64 v[18:19], 11, v[28:29]
	v_lshl_add_u64 v[0:1], s[34:35], 0, v[0:1]
	v_lshl_add_u64 v[18:19], s[34:35], 0, v[18:19]
	v_lshl_add_u64 v[0:1], v[0:1], 0, v[150:151]
	v_lshl_add_u64 v[22:23], v[18:19], 0, v[150:151]
	global_load_dwordx4 v[2:5], v[38:39], off offset:256
	global_load_dwordx4 v[6:9], v[38:39], off offset:288
	global_load_dwordx4 v[10:13], v[38:39], off offset:320
	global_load_dwordx4 v[14:17], v[38:39], off offset:352
	global_load_dwordx4 v[18:21], v[0:1], off
	s_nop 0
	global_load_dwordx4 v[22:25], v[22:23], off
	v_mov_b64_e32 v[0:1], s[6:7]
	v_mad_u64_u32 v[30:31], s[10:11], v26, s46, v[0:1]
	v_mad_i32_i24 v31, v27, s46, v31
	v_lshl_add_u64 v[26:27], v[30:31], 0, v[150:151]
	v_mad_u64_u32 v[30:31], s[10:11], v28, s46, v[0:1]
	v_mad_i32_i24 v31, v29, s46, v31
	v_lshl_add_u64 v[30:31], v[30:31], 0, v[150:151]
	v_lshl_add_u64 v[34:35], s[26:27], 0, v[144:145]
	global_load_dwordx4 v[26:29], v[26:27], off
	s_nop 0
	global_load_dwordx4 v[30:33], v[30:31], off
	v_mad_u64_u32 v[36:37], s[10:11], v34, s46, v[0:1]
	v_mad_i32_i24 v37, v35, s46, v37
	v_lshl_add_u64 v[34:35], v[36:37], 0, v[152:153]
	global_load_dwordx4 v[34:37], v[34:35], off offset:256
	s_nop 0
	global_load_dwordx4 v[124:127], v[38:39], off
	global_load_dwordx4 v[120:123], v[38:39], off offset:32
	global_load_dwordx4 v[116:119], v[38:39], off offset:64
	global_load_dwordx4 v[112:115], v[38:39], off offset:96
	global_load_dwordx4 v[108:111], v[38:39], off offset:128
	global_load_dwordx4 v[104:107], v[38:39], off offset:160
	global_load_dwordx4 v[100:103], v[38:39], off offset:192
	global_load_dwordx4 v[96:99], v[38:39], off offset:224
	s_lshl_b32 s8, s8, 12
	v_add_u32_e32 v190, s8, v166
	v_add_u32_e32 v191, s47, v170
	v_add_u32_e32 v192, s47, v171
	v_add_u32_e32 v193, s47, v172
	v_add_u32_e32 v194, s47, v173
	s_and_b32 s9, s9, 0x3fffffc0
	s_lshl_b32 s9, s9, 2
	s_add_i32 s62, s9, 0
	s_add_i32 s62, s62, 0x14000
	s_mov_b32 s11, s27
	s_mov_b32 s22, s27
	s_mov_b32 s23, s27
	s_mov_b32 s8, s27
	s_mov_b32 s9, s27
	s_mov_b32 s12, s27
	s_mov_b32 s13, s27
	s_mov_b32 s14, s27
	s_mov_b32 s15, s27
	s_mov_b32 s16, s27
	s_mov_b32 s17, s27
	s_mov_b32 s18, s27
	s_mov_b32 s19, s27
	s_mov_b32 s20, s27
	s_mov_b32 s21, s27
	v_add_u32_e32 v195, 0, v168
	s_mov_b32 s64, 2
	v_mov_b32_e32 v140, 0
	v_add_u32_e32 v196, 0x12000, v195
	v_lshrrev_b32_e32 v156, 4, v254
	v_and_b32_e32 v157, 7, v156
	v_and_b32_e32 v159, 15, v254
	v_xor_b32_e32 v157, v157, v159
	v_lshlrev_b32_e32 v157, 4, v157
	v_mad_u32_u24 v154, v156, s46, v157
	v_lshrrev_b32_e32 v156, 3, v254
	v_and_b32_e32 v157, 7, v156
	v_and_b32_e32 v159, 7, v254
	v_xor_b32_e32 v157, v157, v159
	v_lshlrev_b32_e32 v157, 4, v157
	v_add_u32_e32 v157, 0x100, v157
	v_mad_u32_u24 v155, v156, s46, v157
	v_and_b32_e32 v158, 3, v254
	v_lshlrev_b32_e32 v158, 4, v158
	v_bfe_u32 v156, v254, 5, 2
	v_lshl_or_b32 v158, v156, 6, v158
	v_bfe_u32 v156, v254, 2, 2
	v_lshl_or_b32 v158, v156, 11, v158
	v_bfe_u32 v156, v254, 7, 1
	v_lshl_or_b32 v158, v156, 13, v158
	v_bfe_u32 v156, v254, 4, 1
	v_lshl_or_b32 v158, v156, 14, v158
	v_bfe_u32 v156, v254, 8, 1
	v_lshl_or_b32 v158, v156, 15, v158
	v_lshl_add_u32 v189, v188, 2, s62
	s_waitcnt vmcnt(16)
	ds_write_b128 v190, v[2:5]
	s_waitcnt vmcnt(15)
	ds_write_b128 v190, v[6:9] offset:1024
	s_waitcnt vmcnt(14)
	ds_write_b128 v190, v[10:13] offset:2048
	s_waitcnt vmcnt(13)
	ds_write_b128 v190, v[14:17] offset:3072
	s_waitcnt vmcnt(0)
	s_waitcnt vmcnt(12)
	ds_write_b128 v175, v[18:21]
	s_waitcnt vmcnt(11)
	ds_write_b128 v176, v[22:25]
	s_waitcnt vmcnt(10)
	ds_write_b128 v177, v[26:29] offset:32768
	s_waitcnt vmcnt(9)
	ds_write_b128 v178, v[30:33] offset:32768
	s_waitcnt vmcnt(8)
	ds_write_b128 v179, v[34:37]
	s_waitcnt lgkmcnt(0)
	s_barrier
	ds_read_b128 v[2:5], v180 offset:32768
	ds_read_b128 v[6:9], v180 offset:40960
	s_waitcnt vmcnt(7) lgkmcnt(1)
	v_mfma_f32_32x32x16_bf16 v[48:63], v[2:5], v[124:127], 0
	s_waitcnt lgkmcnt(0)
	v_mfma_f32_32x32x16_bf16 v[64:79], v[6:9], v[124:127], 0
	ds_read_b128 v[2:5], v181 offset:32768
	ds_read_b128 v[6:9], v181 offset:40960
	s_waitcnt vmcnt(6) lgkmcnt(1)
	v_mfma_f32_32x32x16_bf16 v[48:63], v[2:5], v[120:123], v[48:63]
	s_waitcnt lgkmcnt(0)
	v_mfma_f32_32x32x16_bf16 v[64:79], v[6:9], v[120:123], v[64:79]
	ds_read_b128 v[2:5], v182 offset:32768
	ds_read_b128 v[6:9], v182 offset:40960
	s_waitcnt vmcnt(5) lgkmcnt(1)
	v_mfma_f32_32x32x16_bf16 v[48:63], v[2:5], v[116:119], v[48:63]
	s_waitcnt lgkmcnt(0)
	v_mfma_f32_32x32x16_bf16 v[64:79], v[6:9], v[116:119], v[64:79]
	ds_read_b128 v[2:5], v183 offset:32768
	ds_read_b128 v[6:9], v183 offset:40960
	s_waitcnt vmcnt(4) lgkmcnt(1)
	v_mfma_f32_32x32x16_bf16 v[48:63], v[2:5], v[112:115], v[48:63]
	s_waitcnt lgkmcnt(0)
	v_mfma_f32_32x32x16_bf16 v[64:79], v[6:9], v[112:115], v[64:79]
	ds_read_b128 v[2:5], v184 offset:32768
	ds_read_b128 v[6:9], v184 offset:40960
	s_waitcnt vmcnt(3) lgkmcnt(1)
	v_mfma_f32_32x32x16_bf16 v[48:63], v[2:5], v[108:111], v[48:63]
	s_waitcnt lgkmcnt(0)
	v_mfma_f32_32x32x16_bf16 v[64:79], v[6:9], v[108:111], v[64:79]
	ds_read_b128 v[2:5], v185 offset:32768
	ds_read_b128 v[6:9], v185 offset:40960
	s_waitcnt vmcnt(2) lgkmcnt(1)
	v_mfma_f32_32x32x16_bf16 v[48:63], v[2:5], v[104:107], v[48:63]
	s_waitcnt lgkmcnt(0)
	v_mfma_f32_32x32x16_bf16 v[64:79], v[6:9], v[104:107], v[64:79]
	ds_read_b128 v[2:5], v186 offset:32768
	ds_read_b128 v[6:9], v186 offset:40960
	s_waitcnt vmcnt(1) lgkmcnt(1)
	v_mfma_f32_32x32x16_bf16 v[48:63], v[2:5], v[100:103], v[48:63]
	s_waitcnt lgkmcnt(0)
	v_mfma_f32_32x32x16_bf16 v[64:79], v[6:9], v[100:103], v[64:79]
	ds_read_b128 v[2:5], v187 offset:32768
	ds_read_b128 v[6:9], v187 offset:40960
	s_waitcnt vmcnt(0) lgkmcnt(1)
	v_mfma_f32_32x32x16_bf16 v[48:63], v[2:5], v[96:99], v[48:63]
	s_waitcnt lgkmcnt(0)
	v_mfma_f32_32x32x16_bf16 v[64:79], v[6:9], v[96:99], v[64:79]
	ds_read_b128 v[2:5], v191
	ds_read_b128 v[6:9], v190
	ds_read_b128 v[10:13], v191 offset:4096
	ds_read_b128 v[14:17], v190 offset:1024
	s_waitcnt lgkmcnt(2)
	v_mfma_f32_32x32x16_bf16 v[48:63], v[2:5], v[6:9], v[48:63]
	s_waitcnt lgkmcnt(1)
	v_mfma_f32_32x32x16_bf16 v[64:79], v[10:13], v[6:9], v[64:79]
	ds_read_b128 v[2:5], v192
	ds_read_b128 v[6:9], v192 offset:4096
	s_waitcnt lgkmcnt(1)
	v_mfma_f32_32x32x16_bf16 v[48:63], v[2:5], v[14:17], v[48:63]
	s_waitcnt lgkmcnt(0)
	v_mfma_f32_32x32x16_bf16 v[64:79], v[6:9], v[14:17], v[64:79]
	ds_read_b128 v[2:5], v193
	ds_read_b128 v[6:9], v190 offset:2048
	ds_read_b128 v[10:13], v193 offset:4096
	ds_read_b128 v[14:17], v190 offset:3072
	s_waitcnt lgkmcnt(2)
	v_mfma_f32_32x32x16_bf16 v[48:63], v[2:5], v[6:9], v[48:63]
	s_waitcnt lgkmcnt(1)
	v_mfma_f32_32x32x16_bf16 v[64:79], v[10:13], v[6:9], v[64:79]
	ds_read_b128 v[2:5], v194
	ds_read_b128 v[6:9], v194 offset:4096
	s_waitcnt lgkmcnt(1)
	v_mfma_f32_32x32x16_bf16 v[48:63], v[2:5], v[14:17], v[48:63]
	s_waitcnt lgkmcnt(0)
	v_mfma_f32_32x32x16_bf16 v[64:79], v[6:9], v[14:17], v[64:79]
	s_nop 9
	v_max_f32_e32 v2, v49, v49
	v_max_f32_e32 v3, v48, v48
	v_max_f32_e32 v2, v3, v2
	v_max3_f32 v2, v2, v50, v51
	v_max3_f32 v2, v2, v52, v53
	v_max3_f32 v2, v2, v54, v55
	v_max3_f32 v2, v2, v56, v57
	v_max3_f32 v2, v2, v58, v59
	v_max3_f32 v2, v2, v60, v61
	v_max3_f32 v2, v2, v62, v63
	v_max3_f32 v2, v2, v64, v65
	v_max3_f32 v2, v2, v66, v67
	v_max3_f32 v2, v2, v68, v69
	v_max3_f32 v2, v2, v70, v71
	v_max3_f32 v2, v2, v72, v73
	v_max3_f32 v2, v2, v74, v75
	v_max3_f32 v2, v2, v76, v77
	v_max3_f32 v2, v2, v78, v79
	v_mov_b32_e32 v3, v2
	s_nop 1
	v_permlane32_swap_b32_e32 v2, v3
	v_max_f32_e32 v3, v3, v3
	v_max_f32_e32 v2, v2, v2
	v_max_f32_e32 v2, v2, v3
	v_add_f32_e32 v3, 0x7149f2ca, v2
	v_cmp_ge_f32_e32 vcc, s48, v3
	s_cmp_eq_u64 vcc, exec
	s_cselect_b64 vcc, -1, 0
	s_add_i32 s10, s26, 64
	v_max_f32_e32 v128, 0xf149f2ca, v2
	v_lshl_add_u64 v[2:3], s[10:11], 0, v[142:143]
	v_lshl_add_u64 v[4:5], v[146:147], 0, s[10:11]
	v_lshl_add_u64 v[6:7], s[10:11], 0, v[144:145]
	v_lshlrev_b64 v[8:9], 11, v[2:3]
	v_lshlrev_b64 v[10:11], 11, v[4:5]
	v_mad_u64_u32 v[12:13], s[10:11], v2, s46, v[0:1]
	v_mad_u64_u32 v[14:15], s[10:11], v4, s46, v[0:1]
	v_mad_u64_u32 v[0:1], s[10:11], v6, s46, v[0:1]
	v_lshl_add_u64 v[8:9], s[34:35], 0, v[8:9]
	v_lshl_add_u64 v[10:11], s[34:35], 0, v[10:11]
	v_mad_i32_i24 v13, v3, s46, v13
	v_mad_i32_i24 v15, v5, s46, v15
	v_mad_i32_i24 v1, v7, s46, v1
	v_lshl_add_u64 v[2:3], v[8:9], 0, v[150:151]
	v_lshl_add_u64 v[4:5], v[10:11], 0, v[150:151]
	v_lshl_add_u64 v[6:7], v[12:13], 0, v[150:151]
	v_lshl_add_u64 v[8:9], v[14:15], 0, v[150:151]
	v_lshl_add_u64 v[0:1], v[0:1], 0, v[152:153]
	global_load_dwordx4 v[80:83], v[2:3], off
	global_load_dwordx4 v[84:87], v[4:5], off
	global_load_dwordx4 v[88:91], v[6:7], off
	global_load_dwordx4 v[92:95], v[8:9], off
	global_load_dwordx4 v[200:203], v[0:1], off offset:256
	v_sub_f32_e32 v129, 0xf149f2ca, v128
	v_mul_f32_e32 v129, 0x3dd53b94, v129
	v_exp_f32_e32 v164, v129
	v_mov_b32_e32 v129, 0xf149f2ca
	v_cndmask_b32_e32 v198, v128, v129, vcc
	v_mul_f32_e32 v138, 0xbdd53b94, v198
	v_mov_b32_e32 v165, v138
	v_fmamk_f32 v48, v48, 0x3dd53b94, v138
	v_fmamk_f32 v49, v49, 0x3dd53b94, v138
	v_fmamk_f32 v50, v50, 0x3dd53b94, v138
	v_fmamk_f32 v51, v51, 0x3dd53b94, v138
	v_fmamk_f32 v52, v52, 0x3dd53b94, v138
	v_fmamk_f32 v53, v53, 0x3dd53b94, v138
	v_fmamk_f32 v54, v54, 0x3dd53b94, v138
	v_fmamk_f32 v55, v55, 0x3dd53b94, v138
	v_fmamk_f32 v56, v56, 0x3dd53b94, v138
	v_fmamk_f32 v57, v57, 0x3dd53b94, v138
	v_fmamk_f32 v58, v58, 0x3dd53b94, v138
	v_fmamk_f32 v59, v59, 0x3dd53b94, v138
	v_fmamk_f32 v60, v60, 0x3dd53b94, v138
	v_fmamk_f32 v61, v61, 0x3dd53b94, v138
	v_fmamk_f32 v62, v62, 0x3dd53b94, v138
	v_fmac_f32_e32 v165, 0x3dd53b94, v63
	s_mov_b32 s10, s27
	s_mov_b32 s11, s27
	v_mov_b64_e32 v[30:31], s[22:23]
	v_exp_f32_e32 v222, v48
	v_exp_f32_e32 v224, v49
	v_exp_f32_e32 v220, v50
	v_exp_f32_e32 v223, v51
	v_exp_f32_e32 v219, v52
	v_exp_f32_e32 v221, v53
	v_exp_f32_e32 v217, v54
	v_exp_f32_e32 v218, v55
	v_exp_f32_e32 v212, v56
	v_exp_f32_e32 v214, v57
	v_exp_f32_e32 v211, v58
	v_exp_f32_e32 v213, v59
	v_exp_f32_e32 v208, v60
	v_exp_f32_e32 v210, v61
	v_exp_f32_e32 v207, v62
	v_exp_f32_e32 v209, v165
	v_mov_b64_e32 v[16:17], s[8:9]
	s_waitcnt vmcnt(0)
	v_mov_b64_e32 v[28:29], s[20:21]
	v_mov_b64_e32 v[26:27], s[18:19]
	v_mov_b64_e32 v[24:25], s[16:17]
	v_mov_b64_e32 v[22:23], s[14:15]
	v_mov_b64_e32 v[20:21], s[12:13]
	v_mov_b64_e32 v[18:19], s[10:11]
	v_mov_b64_e32 v[46:47], v[30:31]
	v_mov_b64_e32 v[0:1], v[16:17]
	v_mov_b64_e32 v[62:63], v[30:31]
	v_mov_b64_e32 v[44:45], v[28:29]
	v_mov_b64_e32 v[42:43], v[26:27]
	v_mov_b64_e32 v[40:41], v[24:25]
	v_mov_b64_e32 v[38:39], v[22:23]
	v_mov_b64_e32 v[36:37], v[20:21]
	v_mov_b64_e32 v[34:35], v[18:19]
	v_mov_b64_e32 v[32:33], v[16:17]
	v_mov_b64_e32 v[2:3], v[18:19]
	v_mov_b64_e32 v[4:5], v[20:21]
	v_mov_b64_e32 v[6:7], v[22:23]
	v_mov_b64_e32 v[8:9], v[24:25]
	v_mov_b64_e32 v[10:11], v[26:27]
	v_mov_b64_e32 v[12:13], v[28:29]
	v_mov_b64_e32 v[14:15], v[30:31]
	s_add_i32 s10, s26, 0x80
	s_add_i32 s83, s26, 64
	s_sub_i32 s11, s65, 64
	v_pk_fma_f32 v[134:135], v[78:79], s[28:29], v[138:139] op_sel_hi:[1,0,0]
	v_pk_fma_f32 v[160:161], v[76:77], s[28:29], v[138:139] op_sel_hi:[1,0,0]
	v_pk_fma_f32 v[162:163], v[74:75], s[28:29], v[138:139] op_sel_hi:[1,0,0]
	v_pk_fma_f32 v[128:129], v[72:73], s[28:29], v[138:139] op_sel_hi:[1,0,0]
	v_pk_fma_f32 v[130:131], v[70:71], s[28:29], v[138:139] op_sel_hi:[1,0,0]
	v_pk_fma_f32 v[132:133], v[68:69], s[28:29], v[138:139] op_sel_hi:[1,0,0]
	v_pk_fma_f32 v[136:137], v[66:67], s[28:29], v[138:139] op_sel_hi:[1,0,0]
	v_pk_fma_f32 v[138:139], v[64:65], s[28:29], v[138:139] op_sel_hi:[1,0,0]
	v_cndmask_b32_e64 v197, v164, 1.0, vcc
	v_mov_b64_e32 v[60:61], v[28:29]
	v_mov_b64_e32 v[58:59], v[26:27]
	v_mov_b64_e32 v[56:57], v[24:25]
	v_mov_b64_e32 v[54:55], v[22:23]
	v_mov_b64_e32 v[52:53], v[20:21]
	v_mov_b64_e32 v[50:51], v[18:19]
	v_mov_b64_e32 v[48:49], v[16:17]
	s_waitcnt vmcnt(4)
	ds_write_b128 v175, v[80:83] offset:16384
	s_waitcnt vmcnt(3)
	ds_write_b128 v176, v[84:87] offset:16384
	s_waitcnt vmcnt(2)
	ds_write_b128 v177, v[88:91] offset:49152
	s_waitcnt vmcnt(1)
	ds_write_b128 v178, v[92:95] offset:49152
	s_waitcnt vmcnt(0)
	ds_write_b128 v196, v[200:203]
	s_waitcnt lgkmcnt(0)
	s_barrier
	s_mov_b32 s80, s10
	s_mul_i32 s81, s80, 0xc00
	s_add_i32 s85, s82, 0x8000
	s_mov_b32 m0, s85
	s_add_i32 s85, s82, 0x10000
	buffer_load_dwordx4 v154, s[72:75], s81 offen lds
	s_mov_b32 m0, s85
	s_add_i32 s85, s82, 0xa000
	buffer_load_dwordx4 v155, s[72:75], s81 offen lds
	s_mov_b32 m0, s85
	s_add_i32 s81, s81, 0x18000
	buffer_load_dwordx4 v154, s[72:75], s81 offen lds
	s_lshl_b32 s81, s83, 11
	s_add_i32 s85, s82, 0x4000
	s_mov_b32 m0, s85
	s_add_i32 s85, s82, 0x6000
	buffer_load_dwordx4 v158, s[76:79], s81 offen lds
	s_mov_b32 m0, s85
	s_add_i32 s81, s81, 0x10000
	buffer_load_dwordx4 v158, s[76:79], s81 offen lds
	s_mov_b32 s84, s80
.LBB0_757:
	s_add_i32 s12, s64, -1
	s_add_i32 s6, 0, 0x12000
	v_add_u32_e32 v199, s6, v170
	v_add_u32_e32 v204, s6, v171
	v_add_u32_e32 v205, s6, v172
	ds_read_b128 v[64:67], v180 offset:49152
	ds_read_b128 v[68:71], v180 offset:57344
	ds_read_b128 v[200:203], v181 offset:49152
	ds_read_b128 v[226:229], v181 offset:57344
	ds_read_b128 v[230:233], v182 offset:49152
	ds_read_b128 v[234:237], v182 offset:57344
	ds_read_b128 v[238:241], v183 offset:49152
	ds_read_b128 v[242:245], v183 offset:57344
	s_waitcnt lgkmcnt(7)
	v_mfma_f32_32x32x16_bf16 v[80:95], v[64:67], v[124:127], 0
	v_exp_f32_e32 v216, v128
	v_add_f32_e32 v128, 0, v222
	v_add_f32_e32 v128, v224, v128
	v_add_f32_e32 v128, v220, v128
	v_add_f32_e32 v128, v223, v128
	v_add_f32_e32 v128, v219, v128
	v_add_f32_e32 v128, v221, v128
	s_waitcnt lgkmcnt(6)
	v_mfma_f32_32x32x16_bf16 v[64:79], v[68:71], v[124:127], 0
	v_add_f32_e32 v128, v217, v128
	v_add_f32_e32 v128, v218, v128
	v_add_f32_e32 v128, v212, v128
	v_add_f32_e32 v128, v214, v128
	v_add_f32_e32 v128, v211, v128
	v_add_f32_e32 v128, v213, v128
	v_exp_f32_e32 v138, v138
	s_waitcnt lgkmcnt(5)
	v_mfma_f32_32x32x16_bf16 v[80:95], v[200:203], v[120:123], v[80:95]
	v_add_f32_e32 v128, v208, v128
	v_exp_f32_e32 v139, v139
	v_add_f32_e32 v128, v210, v128
	v_exp_f32_e32 v164, v136
	v_add_f32_e32 v128, v207, v128
	v_exp_f32_e32 v137, v137
	v_add_f32_e32 v128, v209, v128
	s_waitcnt lgkmcnt(4)
	v_mfma_f32_32x32x16_bf16 v[64:79], v[226:229], v[120:123], v[64:79]
	ds_read_b128 v[200:203], v184 offset:49152
	ds_read_b128 v[226:229], v184 offset:57344
	v_exp_f32_e32 v165, v132
	v_add_f32_e32 v128, v138, v128
	v_add_f32_e32 v128, v139, v128
	v_exp_f32_e32 v206, v130
	v_add_f32_e32 v128, v164, v128
	v_exp_f32_e32 v215, v131
	s_waitcnt lgkmcnt(5)
	v_mfma_f32_32x32x16_bf16 v[80:95], v[230:233], v[116:119], v[80:95]
	v_add_f32_e32 v128, v137, v128
	v_add_f32_e32 v128, v165, v128
	v_exp_f32_e32 v225, v129
	v_exp_f32_e32 v162, v162
	v_exp_f32_e32 v163, v163
	v_exp_f32_e32 v160, v160
	v_exp_f32_e32 v161, v161
	s_waitcnt lgkmcnt(4)
	v_mfma_f32_32x32x16_bf16 v[64:79], v[234:237], v[116:119], v[64:79]
	ds_read_b128 v[230:233], v185 offset:49152
	ds_read_b128 v[234:237], v185 offset:57344
	v_cvt_pk_bf16_f32 v129, v220, v223
	v_cvt_pk_bf16_f32 v130, v219, v221
	v_cvt_pk_bf16_f32 v131, v217, v218
	v_cvt_pk_bf16_f32 v132, v212, v214
	v_cvt_pk_bf16_f32 v136, v138, v139
	v_cvt_pk_bf16_f32 v137, v164, v137
	s_waitcnt lgkmcnt(5)
	v_mfma_f32_32x32x16_bf16 v[80:95], v[238:241], v[112:115], v[80:95]
	v_cvt_pk_bf16_f32 v139, v206, v215
	v_permlane32_swap_b32_e32 v129, v131
	s_nop 0
	v_permlane32_swap_b32_e32 v137, v139
	s_waitcnt lgkmcnt(4)
	v_mfma_f32_32x32x16_bf16 v[64:79], v[242:245], v[112:115], v[64:79]
	ds_read_b128 v[238:241], v186 offset:49152
	ds_read_b128 v[242:245], v186 offset:57344
	s_waitcnt lgkmcnt(5)
	v_mfma_f32_32x32x16_bf16 v[80:95], v[200:203], v[108:111], v[80:95]
	s_waitcnt lgkmcnt(4)
	v_mfma_f32_32x32x16_bf16 v[64:79], v[226:229], v[108:111], v[64:79]
	ds_read_b128 v[200:203], v187 offset:49152
	ds_read_b128 v[226:229], v187 offset:57344
	s_waitcnt lgkmcnt(5)
	v_mfma_f32_32x32x16_bf16 v[80:95], v[230:233], v[104:107], v[80:95]
	s_waitcnt lgkmcnt(4)
	v_mfma_f32_32x32x16_bf16 v[64:79], v[234:237], v[104:107], v[64:79]
	ds_read_b128 v[230:233], v199
	ds_read_b128 v[234:237], v199 offset:4096
	ds_read_b128 v[246:249], v190
	s_waitcnt lgkmcnt(6)
	v_mfma_f32_32x32x16_bf16 v[80:95], v[238:241], v[100:103], v[80:95]
	s_waitcnt lgkmcnt(5)
	v_mfma_f32_32x32x16_bf16 v[64:79], v[242:245], v[100:103], v[64:79]
	ds_read_b128 v[238:241], v204
	ds_read_b128 v[242:245], v204 offset:4096
	ds_read_b128 v[250:253], v190 offset:1024
	v_add_u32_e32 v204, s6, v173
	s_waitcnt lgkmcnt(7)
	v_mfma_f32_32x32x16_bf16 v[80:95], v[200:203], v[96:99], v[80:95]
	s_waitcnt lgkmcnt(6)
	v_mfma_f32_32x32x16_bf16 v[64:79], v[226:229], v[96:99], v[64:79]
	ds_read_b128 v[200:203], v205
	ds_read_b128 v[226:229], v205 offset:4096
	s_waitcnt lgkmcnt(5)
	v_mfma_f32_32x32x16_bf16 v[80:95], v[230:233], v[246:249], v[80:95]
	s_waitcnt lgkmcnt(5)
	v_mfma_f32_32x32x16_bf16 v[64:79], v[234:237], v[246:249], v[64:79]
	ds_read_b128 v[230:233], v204
	ds_read_b128 v[234:237], v204 offset:4096
	ds_read_b128 v[246:249], v190 offset:2048
	s_waitcnt lgkmcnt(5)
	v_mfma_f32_32x32x16_bf16 v[80:95], v[238:241], v[250:253], v[80:95]
	s_waitcnt lgkmcnt(5)
	v_mfma_f32_32x32x16_bf16 v[64:79], v[242:245], v[250:253], v[64:79]
	ds_read_b128 v[250:253], v190 offset:3072
	s_waitcnt lgkmcnt(1)
	v_mfma_f32_32x32x16_bf16 v[80:95], v[200:203], v[246:249], v[80:95]
	v_exp_f32_e32 v205, v133
	v_cvt_pk_bf16_f32 v133, v211, v213
	v_cvt_pk_bf16_f32 v138, v165, v205
	v_add_f32_e32 v128, v205, v128
	v_add_f32_e32 v128, v206, v128
	v_add_f32_e32 v128, v215, v128
	s_waitcnt lgkmcnt(1)
	v_mfma_f32_32x32x16_bf16 v[64:79], v[226:229], v[246:249], v[64:79]
	v_add_f32_e32 v128, v216, v128
	v_add_f32_e32 v128, v225, v128
	v_add_f32_e32 v128, v162, v128
	v_add_f32_e32 v128, v163, v128
	v_add_f32_e32 v128, v160, v128
	v_add_f32_e32 v128, v161, v128
	s_waitcnt lgkmcnt(0)
	v_mfma_f32_32x32x16_bf16 v[80:95], v[230:233], v[250:253], v[80:95]
	v_exp_f32_e32 v226, v134
	v_exp_f32_e32 v227, v135
	v_cvt_pk_bf16_f32 v134, v208, v210
	v_cvt_pk_bf16_f32 v135, v207, v209
	v_add_f32_e32 v128, v226, v128
	v_add_f32_e32 v203, v227, v128
	v_mov_b32_e32 v204, v203
	s_waitcnt lgkmcnt(0)
	v_mfma_f32_32x32x16_bf16 v[64:79], v[234:237], v[250:253], v[64:79]
	s_nop 0
	v_permlane32_swap_b32_e32 v203, v204
	v_cvt_pk_bf16_f32 v128, v222, v224
	v_cvt_pk_bf16_f32 v208, v216, v225
	v_cvt_pk_bf16_f32 v209, v162, v163
	v_cvt_pk_bf16_f32 v210, v160, v161
	v_cvt_pk_bf16_f32 v211, v226, v227
	v_permlane32_swap_b32_e32 v132, v134
	v_permlane32_swap_b32_e32 v128, v130
	v_permlane32_swap_b32_e32 v133, v135
	v_permlane32_swap_b32_e32 v136, v138
	v_permlane32_swap_b32_e32 v208, v210
	v_permlane32_swap_b32_e32 v209, v211
	ds_read_b64_tr_b16 v[160:161], v167 offset:0
	ds_read_b64_tr_b16 v[162:163], v167 offset:0x800
	ds_read_b64_tr_b16 v[232:233], v167 offset:0x1000
	ds_read_b64_tr_b16 v[234:235], v167 offset:0x1800
	ds_read_b64_tr_b16 v[236:237], v167 offset:0x2000
	ds_read_b64_tr_b16 v[238:239], v167 offset:0x2800
	ds_read_b64_tr_b16 v[240:241], v167 offset:0x3000
	ds_read_b64_tr_b16 v[242:243], v167 offset:0x3800
	v_max_f32_e32 v164, v81, v81
	v_max_f32_e32 v165, v80, v80
	v_max_f32_e32 v164, v165, v164
	v_max3_f32 v164, v164, v82, v83
	v_max3_f32 v164, v164, v84, v85
	v_max3_f32 v164, v164, v86, v87
	v_max3_f32 v164, v164, v88, v89
	v_max3_f32 v164, v164, v90, v91
	v_max3_f32 v164, v164, v92, v93
	v_max3_f32 v164, v164, v94, v95
	s_waitcnt lgkmcnt(0)
	v_mfma_f32_32x32x16_bf16 v[16:31], v[128:131], v[160:163], v[16:31]
	v_max3_f32 v160, v164, v64, v65
	v_max3_f32 v160, v160, v66, v67
	v_max3_f32 v160, v160, v68, v69
	v_mfma_f32_32x32x16_bf16 v[16:31], v[132:135], v[232:235], v[16:31]
	ds_read_b64_tr_b16 v[232:233], v167 offset:0x200
	ds_read_b64_tr_b16 v[234:235], v167 offset:0xa00
	v_max3_f32 v160, v160, v70, v71
	v_max3_f32 v160, v160, v72, v73
	v_max3_f32 v160, v160, v74, v75
	v_mfma_f32_32x32x16_bf16 v[16:31], v[136:139], v[236:239], v[16:31]
	ds_read_b64_tr_b16 v[236:237], v167 offset:0x1200
	ds_read_b64_tr_b16 v[238:239], v167 offset:0x1a00
	ds_read_b64_tr_b16 v[244:245], v167 offset:0x2200
	ds_read_b64_tr_b16 v[246:247], v167 offset:0x2a00
	ds_read_b64_tr_b16 v[248:249], v167 offset:0x3200
	ds_read_b64_tr_b16 v[250:251], v167 offset:0x3a00
	v_max3_f32 v160, v160, v76, v77
	v_max3_f32 v160, v160, v78, v79
	v_mov_b32_e32 v161, v160
	v_mfma_f32_32x32x16_bf16 v[16:31], v[208:211], v[240:243], v[16:31]
	v_max_f32_e32 v162, v198, v198
	v_permlane32_swap_b32_e32 v160, v161
	v_max_f32_e32 v161, v161, v161
	v_max_f32_e32 v160, v160, v160
	v_max_f32_e32 v160, v160, v161
	s_waitcnt lgkmcnt(0)
	v_mfma_f32_32x32x16_bf16 v[32:47], v[128:131], v[232:235], v[32:47]
	ds_read_b64_tr_b16 v[232:233], v167 offset:0x400
	ds_read_b64_tr_b16 v[234:235], v167 offset:0xc00
	v_sub_f32_e32 v161, v160, v198
	v_max_f32_e32 v160, v162, v160
	v_sub_f32_e32 v162, v198, v160
	v_mul_f32_e32 v162, 0x3dd53b94, v162
	v_exp_f32_e32 v162, v162
	v_mfma_f32_32x32x16_bf16 v[32:47], v[132:135], v[236:239], v[32:47]
	ds_read_b64_tr_b16 v[236:237], v167 offset:0x1400
	ds_read_b64_tr_b16 v[238:239], v167 offset:0x1c00
	ds_read_b64_tr_b16 v[240:241], v167 offset:0x2400
	ds_read_b64_tr_b16 v[242:243], v167 offset:0x2c00
	v_cmp_ge_f32_e32 vcc, s48, v161
	s_cmp_eq_u64 vcc, exec
	s_cselect_b64 s[6:7], -1, 0
	v_cndmask_b32_e64 v206, v162, 1.0, s[6:7]
	v_cndmask_b32_e64 v160, v160, v198, s[6:7]
	v_mul_f32_e32 v205, 0xbdd53b94, v160
	v_cmp_gt_f32_e32 vcc, 1.0, v206
	v_mfma_f32_32x32x16_bf16 v[32:47], v[136:139], v[244:247], v[32:47]
	ds_read_b64_tr_b16 v[244:245], v167 offset:0x3400
	ds_read_b64_tr_b16 v[246:247], v167 offset:0x3c00
	v_fmamk_f32 v87, v87, 0x3dd53b94, v205
	v_fmamk_f32 v80, v80, 0x3dd53b94, v205
	v_fmamk_f32 v81, v81, 0x3dd53b94, v205
	v_fmamk_f32 v82, v82, 0x3dd53b94, v205
	v_fmamk_f32 v83, v83, 0x3dd53b94, v205
	v_mfma_f32_32x32x16_bf16 v[32:47], v[208:211], v[248:251], v[32:47]
	v_fmamk_f32 v84, v84, 0x3dd53b94, v205
	v_fmamk_f32 v85, v85, 0x3dd53b94, v205
	v_fmamk_f32 v86, v86, 0x3dd53b94, v205
	v_fmamk_f32 v88, v88, 0x3dd53b94, v205
	v_fmamk_f32 v89, v89, 0x3dd53b94, v205
	s_waitcnt lgkmcnt(0)
	v_mfma_f32_32x32x16_bf16 v[0:15], v[128:131], v[232:235], v[0:15]
	ds_read_b64_tr_b16 v[232:233], v167 offset:0x600
	ds_read_b64_tr_b16 v[234:235], v167 offset:0xe00
	v_fmamk_f32 v90, v90, 0x3dd53b94, v205
	v_fmamk_f32 v91, v91, 0x3dd53b94, v205
	v_fmamk_f32 v92, v92, 0x3dd53b94, v205
	v_fmamk_f32 v93, v93, 0x3dd53b94, v205
	v_fmamk_f32 v94, v94, 0x3dd53b94, v205
	v_mfma_f32_32x32x16_bf16 v[0:15], v[132:135], v[236:239], v[0:15]
	ds_read_b64_tr_b16 v[236:237], v167 offset:0x1600
	ds_read_b64_tr_b16 v[238:239], v167 offset:0x1e00
	v_fmamk_f32 v95, v95, 0x3dd53b94, v205
	v_fmamk_f32 v215, v64, 0x3dd53b94, v205
	v_fmamk_f32 v216, v65, 0x3dd53b94, v205
	v_fmamk_f32 v217, v66, 0x3dd53b94, v205
	v_fmamk_f32 v218, v67, 0x3dd53b94, v205
	v_mfma_f32_32x32x16_bf16 v[0:15], v[136:139], v[240:243], v[0:15]
	ds_read_b64_tr_b16 v[240:241], v167 offset:0x2600
	ds_read_b64_tr_b16 v[242:243], v167 offset:0x2e00
	ds_read_b64_tr_b16 v[248:249], v167 offset:0x3600
	ds_read_b64_tr_b16 v[250:251], v167 offset:0x3e00
	v_fmamk_f32 v219, v68, 0x3dd53b94, v205
	v_fmamk_f32 v212, v73, 0x3dd53b94, v205
	v_fmamk_f32 v213, v74, 0x3dd53b94, v205
	v_fmamk_f32 v214, v75, 0x3dd53b94, v205
	v_mfma_f32_32x32x16_bf16 v[0:15], v[208:211], v[244:247], v[0:15]
	v_fmamk_f32 v207, v76, 0x3dd53b94, v205
	v_fmamk_f32 v220, v77, 0x3dd53b94, v205
	v_fmamk_f32 v221, v78, 0x3dd53b94, v205
	s_waitcnt vmcnt(0) lgkmcnt(0)
	s_barrier
	v_mfma_f32_32x32x16_bf16 v[48:63], v[128:131], v[232:235], v[48:63]
	s_add_i32 s80, s10, 64
	s_cmp_lt_u32 s12, 2
	s_cselect_b32 s80, s80, s11
	s_mul_i32 s81, s80, 0xc00
	s_add_i32 s85, s82, 0xc000
	s_mov_b32 m0, s85
	s_add_i32 s85, s82, 0x12000
	buffer_load_dwordx4 v154, s[72:75], s81 offen lds
	v_exp_f32_e32 v128, v80
	v_exp_f32_e32 v129, v82
	v_exp_f32_e32 v130, v84
	v_exp_f32_e32 v131, v86
	v_mfma_f32_32x32x16_bf16 v[48:63], v[132:135], v[236:239], v[48:63]
	s_mov_b32 m0, s85
	s_add_i32 s85, s82, 0xe000
	buffer_load_dwordx4 v155, s[72:75], s81 offen lds
	v_exp_f32_e32 v132, v88
	v_exp_f32_e32 v133, v90
	v_exp_f32_e32 v134, v92
	v_exp_f32_e32 v135, v94
	v_mfma_f32_32x32x16_bf16 v[48:63], v[136:139], v[240:243], v[48:63]
	s_mov_b32 m0, s85
	s_add_i32 s81, s81, 0x18000
	buffer_load_dwordx4 v154, s[72:75], s81 offen lds
	v_exp_f32_e32 v139, v89
	v_exp_f32_e32 v138, v91
	v_exp_f32_e32 v137, v93
	v_exp_f32_e32 v136, v95
	v_mfma_f32_32x32x16_bf16 v[48:63], v[208:211], v[248:251], v[48:63]
	s_lshl_b32 s81, s84, 11
	s_add_i32 s85, s82, 0x0
	s_mov_b32 m0, s85
	s_add_i32 s85, s82, 0x2000
	buffer_load_dwordx4 v158, s[76:79], s81 offen lds
	s_mov_b32 m0, s85
	s_add_i32 s81, s81, 0x10000
	buffer_load_dwordx4 v158, s[76:79], s81 offen lds
	s_mov_b32 s83, s80
	v_exp_f32_e32 v161, v87
	v_exp_f32_e32 v198, v81
	v_exp_f32_e32 v163, v83
	v_exp_f32_e32 v162, v85
	v_fmamk_f32 v208, v69, 0x3dd53b94, v205
	v_fmamk_f32 v209, v70, 0x3dd53b94, v205
	v_fmamk_f32 v210, v71, 0x3dd53b94, v205
	v_fmamk_f32 v211, v72, 0x3dd53b94, v205
	v_fmac_f32_e32 v205, 0x3dd53b94, v79
	s_cbranch_vccz .LBB0_761
	s_and_saveexec_b64 s[8:9], s[4:5]
	ds_write_b32 v189, v206 offset:128
	s_or_b64 exec, exec, s[8:9]
	s_waitcnt lgkmcnt(0)
	v_add_u32_e32 v248, s62, v169
	ds_read_b128 v[232:235], v248 offset:224
	ds_read_b128 v[236:239], v248 offset:192
	ds_read_b128 v[240:243], v248 offset:160
	ds_read_b128 v[244:247], v248 offset:128
	s_waitcnt lgkmcnt(3)
	v_pk_mul_f32 v[28:29], v[28:29], v[232:233]
	s_waitcnt lgkmcnt(2)
	v_pk_mul_f32 v[24:25], v[24:25], v[236:237]
	s_waitcnt lgkmcnt(1)
	v_pk_mul_f32 v[20:21], v[20:21], v[240:241]
	v_pk_mul_f32 v[30:31], v[30:31], v[234:235]
	v_pk_mul_f32 v[26:27], v[26:27], v[238:239]
	v_pk_mul_f32 v[22:23], v[22:23], v[242:243]
	s_waitcnt lgkmcnt(0)
	v_pk_mul_f32 v[18:19], v[18:19], v[246:247]
	v_pk_mul_f32 v[16:17], v[16:17], v[244:245]
	v_pk_mul_f32 v[44:45], v[44:45], v[232:233]
	v_pk_mul_f32 v[40:41], v[40:41], v[236:237]
	v_pk_mul_f32 v[36:37], v[36:37], v[240:241]
	v_pk_mul_f32 v[46:47], v[46:47], v[234:235]
	v_pk_mul_f32 v[42:43], v[42:43], v[238:239]
	v_pk_mul_f32 v[38:39], v[38:39], v[242:243]
	v_pk_mul_f32 v[34:35], v[34:35], v[246:247]
	v_pk_mul_f32 v[32:33], v[32:33], v[244:245]
	v_pk_mul_f32 v[12:13], v[12:13], v[232:233]
	v_pk_mul_f32 v[8:9], v[8:9], v[236:237]
	v_pk_mul_f32 v[4:5], v[4:5], v[240:241]
	v_pk_mul_f32 v[14:15], v[14:15], v[234:235]
	v_pk_mul_f32 v[10:11], v[10:11], v[238:239]
	v_pk_mul_f32 v[6:7], v[6:7], v[242:243]
	v_pk_mul_f32 v[2:3], v[2:3], v[246:247]
	v_pk_mul_f32 v[0:1], v[0:1], v[244:245]
	v_pk_mul_f32 v[60:61], v[60:61], v[232:233]
	v_pk_mul_f32 v[56:57], v[56:57], v[236:237]
	v_pk_mul_f32 v[52:53], v[52:53], v[240:241]
	v_pk_mul_f32 v[62:63], v[62:63], v[234:235]
	v_pk_mul_f32 v[58:59], v[58:59], v[238:239]
	v_pk_mul_f32 v[54:55], v[54:55], v[242:243]
	v_pk_mul_f32 v[50:51], v[50:51], v[246:247]
	v_pk_mul_f32 v[48:49], v[48:49], v[244:245]
.LBB0_761:
	ds_read_b128 v[64:67], v180 offset:32768
	ds_read_b128 v[68:71], v180 offset:40960
	ds_read_b128 v[222:225], v181 offset:32768
	ds_read_b128 v[226:229], v181 offset:40960
	ds_read_b128 v[230:233], v182 offset:32768
	ds_read_b128 v[234:237], v182 offset:40960
	ds_read_b128 v[238:241], v183 offset:32768
	ds_read_b128 v[242:245], v183 offset:40960
	v_exp_f32_e32 v164, v215
	v_add_f32_e32 v215, 0, v128
	s_waitcnt lgkmcnt(7)
	v_mfma_f32_32x32x16_bf16 v[80:95], v[64:67], v[124:127], 0
	v_add_f32_e32 v215, v198, v215
	v_add_f32_e32 v215, v129, v215
	v_add_f32_e32 v215, v163, v215
	v_add_f32_e32 v215, v130, v215
	v_add_f32_e32 v215, v162, v215
	v_add_f32_e32 v215, v131, v215
	v_add_f32_e32 v215, v161, v215
	s_waitcnt lgkmcnt(6)
	v_mfma_f32_32x32x16_bf16 v[64:79], v[68:71], v[124:127], 0
	v_add_f32_e32 v215, v132, v215
	v_add_f32_e32 v215, v139, v215
	v_add_f32_e32 v215, v133, v215
	v_add_f32_e32 v215, v138, v215
	v_add_f32_e32 v215, v134, v215
	v_exp_f32_e32 v165, v216
	v_add_f32_e32 v215, v137, v215
	s_waitcnt lgkmcnt(5)
	v_mfma_f32_32x32x16_bf16 v[80:95], v[222:225], v[120:123], v[80:95]
	v_exp_f32_e32 v217, v217
	v_add_f32_e32 v215, v135, v215
	v_exp_f32_e32 v218, v218
	v_add_f32_e32 v215, v136, v215
	v_exp_f32_e32 v219, v219
	v_add_f32_e32 v215, v164, v215
	v_exp_f32_e32 v208, v208
	s_waitcnt lgkmcnt(4)
	v_mfma_f32_32x32x16_bf16 v[64:79], v[226:229], v[120:123], v[64:79]
	ds_read_b128 v[222:225], v184 offset:32768
	ds_read_b128 v[226:229], v184 offset:40960
	v_add_f32_e32 v215, v165, v215
	v_exp_f32_e32 v209, v209
	v_add_f32_e32 v215, v217, v215
	v_exp_f32_e32 v210, v210
	v_add_f32_e32 v215, v218, v215
	v_exp_f32_e32 v211, v211
	s_waitcnt lgkmcnt(5)
	v_mfma_f32_32x32x16_bf16 v[80:95], v[230:233], v[116:119], v[80:95]
	v_add_f32_e32 v215, v219, v215
	v_exp_f32_e32 v212, v212
	v_add_f32_e32 v215, v208, v215
	v_exp_f32_e32 v213, v213
	v_add_f32_e32 v215, v209, v215
	v_exp_f32_e32 v214, v214
	v_add_f32_e32 v215, v210, v215
	s_waitcnt lgkmcnt(4)
	v_mfma_f32_32x32x16_bf16 v[64:79], v[234:237], v[116:119], v[64:79]
	ds_read_b128 v[230:233], v185 offset:32768
	ds_read_b128 v[234:237], v185 offset:40960
	v_exp_f32_e32 v207, v207
	v_add_f32_e32 v215, v211, v215
	v_exp_f32_e32 v220, v220
	v_add_f32_e32 v215, v212, v215
	v_exp_f32_e32 v221, v221
	v_add_f32_e32 v215, v213, v215
	s_waitcnt lgkmcnt(5)
	v_mfma_f32_32x32x16_bf16 v[80:95], v[238:241], v[112:115], v[80:95]
	v_exp_f32_e32 v205, v205
	v_add_f32_e32 v215, v214, v215
	v_add_f32_e32 v215, v207, v215
	v_add_f32_e32 v215, v220, v215
	v_add_f32_e32 v215, v221, v215
	v_add_f32_e32 v215, v205, v215
	v_mov_b32_e32 v216, v215
	s_waitcnt lgkmcnt(4)
	v_mfma_f32_32x32x16_bf16 v[64:79], v[242:245], v[112:115], v[64:79]
	ds_read_b128 v[238:241], v186 offset:32768
	ds_read_b128 v[242:245], v186 offset:40960
	v_permlane32_swap_b32_e32 v215, v216
	v_cvt_pk_bf16_f32 v128, v128, v198
	v_cvt_pk_bf16_f32 v129, v129, v163
	v_cvt_pk_bf16_f32 v130, v130, v162
	v_cvt_pk_bf16_f32 v131, v131, v161
	s_waitcnt lgkmcnt(5)
	v_mfma_f32_32x32x16_bf16 v[80:95], v[222:225], v[108:111], v[80:95]
	v_cvt_pk_bf16_f32 v132, v132, v139
	v_cvt_pk_bf16_f32 v133, v133, v138
	v_cvt_pk_bf16_f32 v134, v134, v137
	v_cvt_pk_bf16_f32 v135, v135, v136
	v_cvt_pk_bf16_f32 v136, v164, v165
	v_cvt_pk_bf16_f32 v137, v217, v218
	v_cvt_pk_bf16_f32 v138, v219, v208
	s_waitcnt lgkmcnt(4)
	v_mfma_f32_32x32x16_bf16 v[64:79], v[226:229], v[108:111], v[64:79]
	ds_read_b128 v[222:225], v187 offset:32768
	ds_read_b128 v[226:229], v187 offset:40960
	v_cvt_pk_bf16_f32 v139, v209, v210
	v_cvt_pk_bf16_f32 v208, v211, v212
	v_cvt_pk_bf16_f32 v209, v213, v214
	v_cvt_pk_bf16_f32 v210, v207, v220
	v_cvt_pk_bf16_f32 v211, v221, v205
	v_permlane32_swap_b32_e32 v128, v130
	s_waitcnt lgkmcnt(5)
	v_mfma_f32_32x32x16_bf16 v[80:95], v[230:233], v[104:107], v[80:95]
	v_permlane32_swap_b32_e32 v129, v131
	v_permlane32_swap_b32_e32 v132, v134
	v_permlane32_swap_b32_e32 v133, v135
	v_permlane32_swap_b32_e32 v136, v138
	s_waitcnt lgkmcnt(4)
	v_mfma_f32_32x32x16_bf16 v[64:79], v[234:237], v[104:107], v[64:79]
	ds_read_b128 v[230:233], v191
	ds_read_b128 v[234:237], v191 offset:4096
	ds_read_b128 v[246:249], v190
	v_permlane32_swap_b32_e32 v137, v139
	v_permlane32_swap_b32_e32 v208, v210
	v_permlane32_swap_b32_e32 v209, v211
	s_waitcnt lgkmcnt(6)
	v_mfma_f32_32x32x16_bf16 v[80:95], v[238:241], v[100:103], v[80:95]
	s_waitcnt lgkmcnt(5)
	v_mfma_f32_32x32x16_bf16 v[64:79], v[242:245], v[100:103], v[64:79]
	ds_read_b128 v[238:241], v192
	ds_read_b128 v[242:245], v192 offset:4096
	ds_read_b128 v[250:253], v190 offset:1024
	s_waitcnt lgkmcnt(7)
	v_mfma_f32_32x32x16_bf16 v[80:95], v[222:225], v[96:99], v[80:95]
	s_waitcnt lgkmcnt(6)
	v_mfma_f32_32x32x16_bf16 v[64:79], v[226:229], v[96:99], v[64:79]
	ds_read_b128 v[222:225], v193
	ds_read_b128 v[226:229], v193 offset:4096
	s_waitcnt lgkmcnt(5)
	v_mfma_f32_32x32x16_bf16 v[80:95], v[230:233], v[246:249], v[80:95]
	s_waitcnt lgkmcnt(5)
	v_mfma_f32_32x32x16_bf16 v[64:79], v[234:237], v[246:249], v[64:79]
	ds_read_b128 v[230:233], v194
	ds_read_b128 v[234:237], v194 offset:4096
	ds_read_b128 v[246:249], v190 offset:2048
	s_waitcnt lgkmcnt(5)
	v_mfma_f32_32x32x16_bf16 v[80:95], v[238:241], v[250:253], v[80:95]
	s_waitcnt lgkmcnt(5)
	v_mfma_f32_32x32x16_bf16 v[64:79], v[242:245], v[250:253], v[64:79]
	ds_read_b128 v[250:253], v190 offset:3072
	s_waitcnt lgkmcnt(1)
	v_mfma_f32_32x32x16_bf16 v[80:95], v[222:225], v[246:249], v[80:95]
	s_waitcnt lgkmcnt(1)
	v_mfma_f32_32x32x16_bf16 v[64:79], v[226:229], v[246:249], v[64:79]
	s_waitcnt lgkmcnt(0)
	v_mfma_f32_32x32x16_bf16 v[80:95], v[230:233], v[250:253], v[80:95]
	s_waitcnt lgkmcnt(0)
	v_mfma_f32_32x32x16_bf16 v[64:79], v[234:237], v[250:253], v[64:79]
	ds_read_b64_tr_b16 v[238:239], v174 offset:0
	ds_read_b64_tr_b16 v[240:241], v174 offset:0x800
	ds_read_b64_tr_b16 v[242:243], v174 offset:0x1000
	ds_read_b64_tr_b16 v[244:245], v174 offset:0x1800
	ds_read_b64_tr_b16 v[246:247], v174 offset:0x2000
	ds_read_b64_tr_b16 v[248:249], v174 offset:0x2800
	ds_read_b64_tr_b16 v[250:251], v174 offset:0x3000
	ds_read_b64_tr_b16 v[252:253], v174 offset:0x3800
	s_nop 3
	v_max_f32_e32 v161, v81, v81
	v_max_f32_e32 v162, v80, v80
	v_max_f32_e32 v161, v162, v161
	v_max3_f32 v161, v161, v82, v83
	v_max3_f32 v161, v161, v84, v85
	v_max3_f32 v161, v161, v86, v87
	v_max3_f32 v161, v161, v88, v89
	v_max3_f32 v161, v161, v90, v91
	v_max3_f32 v161, v161, v92, v93
	v_max3_f32 v161, v161, v94, v95
	s_waitcnt lgkmcnt(0)
	v_mfma_f32_32x32x16_bf16 v[16:31], v[128:131], v[238:241], v[16:31]
	ds_read_b64_tr_b16 v[238:239], v174 offset:0x200
	ds_read_b64_tr_b16 v[240:241], v174 offset:0xa00
	v_max3_f32 v161, v161, v64, v65
	v_max3_f32 v161, v161, v66, v67
	v_max3_f32 v161, v161, v68, v69
	v_mfma_f32_32x32x16_bf16 v[16:31], v[132:135], v[242:245], v[16:31]
	ds_read_b64_tr_b16 v[242:243], v174 offset:0x1200
	ds_read_b64_tr_b16 v[244:245], v174 offset:0x1a00
	v_max3_f32 v161, v161, v70, v71
	v_max3_f32 v161, v161, v72, v73
	v_max3_f32 v161, v161, v74, v75
	v_mfma_f32_32x32x16_bf16 v[16:31], v[136:139], v[246:249], v[16:31]
	ds_read_b64_tr_b16 v[246:247], v174 offset:0x2200
	ds_read_b64_tr_b16 v[248:249], v174 offset:0x2a00
	ds_read_b64_tr_b16 v[162:163], v174 offset:0x3200
	ds_read_b64_tr_b16 v[164:165], v174 offset:0x3a00
	v_max3_f32 v161, v161, v76, v77
	v_max3_f32 v161, v161, v78, v79
	v_mov_b32_e32 v198, v161
	v_mfma_f32_32x32x16_bf16 v[16:31], v[208:211], v[250:253], v[16:31]
	v_max_f32_e32 v205, v160, v160
	v_permlane32_swap_b32_e32 v161, v198
	v_max_f32_e32 v198, v198, v198
	v_max_f32_e32 v161, v161, v161
	v_max_f32_e32 v161, v161, v198
	s_waitcnt lgkmcnt(0)
	v_mfma_f32_32x32x16_bf16 v[32:47], v[128:131], v[238:241], v[32:47]
	ds_read_b64_tr_b16 v[238:239], v174 offset:0x400
	ds_read_b64_tr_b16 v[240:241], v174 offset:0xc00
	v_sub_f32_e32 v198, v161, v160
	v_max_f32_e32 v161, v205, v161
	v_sub_f32_e32 v205, v160, v161
	v_mul_f32_e32 v205, 0x3dd53b94, v205
	v_exp_f32_e32 v205, v205
	v_mfma_f32_32x32x16_bf16 v[32:47], v[132:135], v[242:245], v[32:47]
	ds_read_b64_tr_b16 v[242:243], v174 offset:0x1400
	ds_read_b64_tr_b16 v[244:245], v174 offset:0x1c00
	v_cmp_ge_f32_e32 vcc, s48, v198
	s_cmp_eq_u64 vcc, exec
	s_cselect_b64 s[6:7], -1, 0
	v_cndmask_b32_e64 v205, v205, 1.0, s[6:7]
	v_cndmask_b32_e64 v198, v161, v160, s[6:7]
	v_mul_f32_e32 v236, 0xbdd53b94, v198
	v_mov_b32_e32 v237, v236
	v_cmp_gt_f32_e32 vcc, 1.0, v205
	v_mfma_f32_32x32x16_bf16 v[32:47], v[136:139], v[246:249], v[32:47]
	ds_read_b64_tr_b16 v[246:247], v174 offset:0x2400
	ds_read_b64_tr_b16 v[248:249], v174 offset:0x2c00
	ds_read_b64_tr_b16 v[250:251], v174 offset:0x3400
	ds_read_b64_tr_b16 v[252:253], v174 offset:0x3c00
	v_fmamk_f32 v80, v80, 0x3dd53b94, v236
	v_fmamk_f32 v81, v81, 0x3dd53b94, v236
	v_fmamk_f32 v82, v82, 0x3dd53b94, v236
	v_fmamk_f32 v83, v83, 0x3dd53b94, v236
	v_mfma_f32_32x32x16_bf16 v[32:47], v[208:211], v[162:165], v[32:47]
	v_fmamk_f32 v84, v84, 0x3dd53b94, v236
	v_fmamk_f32 v85, v85, 0x3dd53b94, v236
	v_fmamk_f32 v86, v86, 0x3dd53b94, v236
	v_fmamk_f32 v87, v87, 0x3dd53b94, v236
	s_waitcnt lgkmcnt(0)
	v_mfma_f32_32x32x16_bf16 v[0:15], v[128:131], v[238:241], v[0:15]
	ds_read_b64_tr_b16 v[162:163], v174 offset:0x600
	ds_read_b64_tr_b16 v[164:165], v174 offset:0xe00
	ds_read_b64_tr_b16 v[238:239], v174 offset:0x1600
	ds_read_b64_tr_b16 v[240:241], v174 offset:0x1e00
	v_fmamk_f32 v88, v88, 0x3dd53b94, v236
	v_fmamk_f32 v89, v89, 0x3dd53b94, v236
	v_fmamk_f32 v90, v90, 0x3dd53b94, v236
	v_fmamk_f32 v91, v91, 0x3dd53b94, v236
	v_mfma_f32_32x32x16_bf16 v[0:15], v[132:135], v[242:245], v[0:15]
	ds_read_b64_tr_b16 v[242:243], v174 offset:0x2600
	ds_read_b64_tr_b16 v[244:245], v174 offset:0x2e00
	v_fmamk_f32 v92, v92, 0x3dd53b94, v236
	v_fmamk_f32 v93, v93, 0x3dd53b94, v236
	v_fmamk_f32 v94, v94, 0x3dd53b94, v236
	v_fmamk_f32 v95, v95, 0x3dd53b94, v236
	v_mfma_f32_32x32x16_bf16 v[0:15], v[136:139], v[246:249], v[0:15]
	ds_read_b64_tr_b16 v[246:247], v174 offset:0x3600
	ds_read_b64_tr_b16 v[248:249], v174 offset:0x3e00
	v_exp_f32_e32 v222, v80
	v_exp_f32_e32 v224, v81
	v_exp_f32_e32 v220, v82
	v_mfma_f32_32x32x16_bf16 v[0:15], v[208:211], v[250:253], v[0:15]
	v_exp_f32_e32 v223, v83
	v_exp_f32_e32 v219, v84
	v_exp_f32_e32 v221, v85
	s_waitcnt vmcnt(0) lgkmcnt(0)
	s_barrier
	v_mfma_f32_32x32x16_bf16 v[48:63], v[128:131], v[162:165], v[48:63]
	s_addk_i32 s10, 0x80
	s_add_i32 s64, s64, 2
	s_addk_i32 s11, 0x80
	s_sub_i32 s80, s11, 64
	s_mul_i32 s81, s80, 0xc00
	s_add_i32 s85, s82, 0x8000
	s_mov_b32 m0, s85
	s_add_i32 s85, s82, 0x10000
	buffer_load_dwordx4 v154, s[72:75], s81 offen lds
	v_exp_f32_e32 v217, v86
	v_exp_f32_e32 v218, v87
	v_exp_f32_e32 v212, v88
	v_pk_fma_f32 v[130:131], v[70:71], s[28:29], v[236:237] op_sel_hi:[1,0,0]
	v_pk_fma_f32 v[128:129], v[72:73], s[28:29], v[236:237] op_sel_hi:[1,0,0]
	v_mfma_f32_32x32x16_bf16 v[48:63], v[132:135], v[238:241], v[48:63]
	s_mov_b32 m0, s85
	s_add_i32 s85, s82, 0xa000
	buffer_load_dwordx4 v155, s[72:75], s81 offen lds
	v_exp_f32_e32 v214, v89
	v_exp_f32_e32 v213, v91
	v_exp_f32_e32 v207, v94
	v_pk_fma_f32 v[132:133], v[68:69], s[28:29], v[236:237] op_sel_hi:[1,0,0]
	v_pk_fma_f32 v[134:135], v[78:79], s[28:29], v[236:237] op_sel_hi:[1,0,0]
	v_mfma_f32_32x32x16_bf16 v[48:63], v[136:139], v[242:245], v[48:63]
	s_mov_b32 m0, s85
	s_add_i32 s81, s81, 0x18000
	buffer_load_dwordx4 v154, s[72:75], s81 offen lds
	v_pk_fma_f32 v[138:139], v[64:65], s[28:29], v[236:237] op_sel_hi:[1,0,0]
	v_pk_fma_f32 v[136:137], v[66:67], s[28:29], v[236:237] op_sel_hi:[1,0,0]
	v_pk_fma_f32 v[162:163], v[74:75], s[28:29], v[236:237] op_sel_hi:[1,0,0]
	v_pk_fma_f32 v[160:161], v[76:77], s[28:29], v[236:237] op_sel_hi:[1,0,0]
	v_mfma_f32_32x32x16_bf16 v[48:63], v[208:211], v[246:249], v[48:63]
	s_lshl_b32 s81, s83, 11
	s_add_i32 s85, s82, 0x4000
	s_mov_b32 m0, s85
	s_add_i32 s85, s82, 0x6000
	buffer_load_dwordx4 v158, s[76:79], s81 offen lds
	s_mov_b32 m0, s85
	s_add_i32 s81, s81, 0x10000
	buffer_load_dwordx4 v158, s[76:79], s81 offen lds
	s_mov_b32 s84, s80
	v_exp_f32_e32 v211, v90
	v_exp_f32_e32 v208, v92
	v_exp_f32_e32 v210, v93
	v_exp_f32_e32 v209, v95
	v_add_f32_e32 v64, v203, v204
	v_fmac_f32_e32 v64, v197, v140
	v_add_f32_e32 v140, v215, v216
	v_fmac_f32_e32 v140, v64, v206
	s_cbranch_vccz .LBB0_765
	s_and_saveexec_b64 s[8:9], s[4:5]
	ds_write_b32 v189, v205 offset:128
	s_or_b64 exec, exec, s[8:9]
	s_waitcnt lgkmcnt(0)
	v_add_u32_e32 v164, s62, v169
	ds_read_b128 v[238:241], v164 offset:224
	ds_read_b128 v[242:245], v164 offset:192
	ds_read_b128 v[246:249], v164 offset:160
	ds_read_b128 v[250:253], v164 offset:128
	s_waitcnt lgkmcnt(3)
	v_pk_mul_f32 v[28:29], v[28:29], v[238:239]
	s_waitcnt lgkmcnt(2)
	v_pk_mul_f32 v[24:25], v[24:25], v[242:243]
	s_waitcnt lgkmcnt(1)
	v_pk_mul_f32 v[20:21], v[20:21], v[246:247]
	v_pk_mul_f32 v[30:31], v[30:31], v[240:241]
	v_pk_mul_f32 v[26:27], v[26:27], v[244:245]
	v_pk_mul_f32 v[22:23], v[22:23], v[248:249]
	s_waitcnt lgkmcnt(0)
	v_pk_mul_f32 v[18:19], v[18:19], v[252:253]
	v_pk_mul_f32 v[16:17], v[16:17], v[250:251]
	v_pk_mul_f32 v[44:45], v[44:45], v[238:239]
	v_pk_mul_f32 v[40:41], v[40:41], v[242:243]
	v_pk_mul_f32 v[36:37], v[36:37], v[246:247]
	v_pk_mul_f32 v[46:47], v[46:47], v[240:241]
	v_pk_mul_f32 v[42:43], v[42:43], v[244:245]
	v_pk_mul_f32 v[38:39], v[38:39], v[248:249]
	v_pk_mul_f32 v[34:35], v[34:35], v[252:253]
	v_pk_mul_f32 v[32:33], v[32:33], v[250:251]
	v_pk_mul_f32 v[12:13], v[12:13], v[238:239]
	v_pk_mul_f32 v[8:9], v[8:9], v[242:243]
	v_pk_mul_f32 v[4:5], v[4:5], v[246:247]
	v_pk_mul_f32 v[14:15], v[14:15], v[240:241]
	v_pk_mul_f32 v[10:11], v[10:11], v[244:245]
	v_pk_mul_f32 v[6:7], v[6:7], v[248:249]
	v_pk_mul_f32 v[2:3], v[2:3], v[252:253]
	v_pk_mul_f32 v[0:1], v[0:1], v[250:251]
	v_pk_mul_f32 v[60:61], v[60:61], v[238:239]
	v_pk_mul_f32 v[56:57], v[56:57], v[242:243]
	v_pk_mul_f32 v[52:53], v[52:53], v[246:247]
	v_pk_mul_f32 v[62:63], v[62:63], v[240:241]
	v_pk_mul_f32 v[58:59], v[58:59], v[244:245]
	v_pk_mul_f32 v[54:55], v[54:55], v[248:249]
	v_pk_mul_f32 v[50:51], v[50:51], v[252:253]
	v_pk_mul_f32 v[48:49], v[48:49], v[250:251]
.LBB0_765:
	s_cmp_ge_u32 s64, s63
	s_cbranch_scc1 .LBB0_767
	v_mov_b32_e32 v197, v205
	s_branch .LBB0_757
.LBB0_767:
	ds_read_b128 v[64:67], v180 offset:49152
	ds_read_b128 v[68:71], v180 offset:57344
	v_exp_f32_e32 v138, v138
	v_exp_f32_e32 v139, v139
	v_exp_f32_e32 v136, v136
	s_waitcnt lgkmcnt(1)
	v_mfma_f32_32x32x16_bf16 v[80:95], v[64:67], v[124:127], 0
	v_exp_f32_e32 v137, v137
	v_exp_f32_e32 v132, v132
	v_exp_f32_e32 v128, v128
	v_exp_f32_e32 v129, v129
	s_waitcnt lgkmcnt(0)
	v_mfma_f32_32x32x16_bf16 v[64:79], v[68:71], v[124:127], 0
	ds_read_b128 v[124:127], v181 offset:49152
	ds_read_b128 v[154:157], v181 offset:57344
	s_waitcnt lgkmcnt(1)
	v_mfma_f32_32x32x16_bf16 v[80:95], v[124:127], v[120:123], v[80:95]
	s_waitcnt lgkmcnt(0)
	v_mfma_f32_32x32x16_bf16 v[64:79], v[154:157], v[120:123], v[64:79]
	ds_read_b128 v[120:123], v182 offset:49152
	ds_read_b128 v[124:127], v182 offset:57344
	s_waitcnt lgkmcnt(1)
	v_mfma_f32_32x32x16_bf16 v[80:95], v[120:123], v[116:119], v[80:95]
	s_waitcnt lgkmcnt(0)
	v_mfma_f32_32x32x16_bf16 v[64:79], v[124:127], v[116:119], v[64:79]
	ds_read_b128 v[116:119], v183 offset:49152
	ds_read_b128 v[120:123], v183 offset:57344
	s_waitcnt lgkmcnt(1)
	v_mfma_f32_32x32x16_bf16 v[80:95], v[116:119], v[112:115], v[80:95]
	s_waitcnt lgkmcnt(0)
	v_mfma_f32_32x32x16_bf16 v[64:79], v[120:123], v[112:115], v[64:79]
	ds_read_b128 v[112:115], v184 offset:49152
	ds_read_b128 v[116:119], v184 offset:57344
	s_waitcnt lgkmcnt(1)
	v_mfma_f32_32x32x16_bf16 v[80:95], v[112:115], v[108:111], v[80:95]
	ds_read_b128 v[112:115], v185 offset:49152
	s_waitcnt lgkmcnt(1)
	v_mfma_f32_32x32x16_bf16 v[64:79], v[116:119], v[108:111], v[64:79]
	ds_read_b128 v[108:111], v185 offset:57344
	ds_read_b128 v[116:119], v186 offset:49152
	ds_read_b128 v[120:123], v186 offset:57344
	ds_read_b128 v[124:127], v187 offset:49152
	ds_read_b128 v[154:157], v187 offset:57344
	ds_read_b128 v[192:195], v199
	ds_read_b128 v[226:229], v199 offset:4096
	s_waitcnt lgkmcnt(7)
	v_mfma_f32_32x32x16_bf16 v[80:95], v[112:115], v[104:107], v[80:95]
	ds_read_b128 v[112:115], v200
	ds_read_b128 v[230:233], v200 offset:4096
	ds_read_b128 v[234:237], v190
	ds_read_b128 v[238:241], v190 offset:1024
	ds_read_b128 v[242:245], v201
	ds_read_b128 v[246:249], v201 offset:4096
	ds_read_b128 v[250:253], v202
	ds_read_b128 v[200:203], v202 offset:4096
	s_waitcnt lgkmcnt(14)
	v_mfma_f32_32x32x16_bf16 v[64:79], v[108:111], v[104:107], v[64:79]
	ds_read_b128 v[104:107], v190 offset:2048
	ds_read_b128 v[108:111], v190 offset:3072
	s_waitcnt lgkmcnt(14)
	v_mfma_f32_32x32x16_bf16 v[80:95], v[116:119], v[100:103], v[80:95]
	v_exp_f32_e32 v118, v133
	v_exp_f32_e32 v119, v130
	v_exp_f32_e32 v130, v131
	v_exp_f32_e32 v131, v162
	v_exp_f32_e32 v133, v163
	v_cvt_pk_bf16_f32 v116, v138, v139
	v_cvt_pk_bf16_f32 v117, v136, v137
	v_mfma_f32_32x32x16_bf16 v[64:79], v[120:123], v[100:103], v[64:79]
	v_add_f32_e32 v100, 0, v222
	v_add_f32_e32 v100, v224, v100
	v_add_f32_e32 v100, v220, v100
	v_add_f32_e32 v100, v223, v100
	v_add_f32_e32 v100, v219, v100
	v_add_f32_e32 v100, v221, v100
	v_add_f32_e32 v100, v217, v100
	s_waitcnt lgkmcnt(13)
	v_mfma_f32_32x32x16_bf16 v[80:95], v[124:127], v[96:99], v[80:95]
	v_add_f32_e32 v100, v218, v100
	v_add_f32_e32 v100, v212, v100
	v_add_f32_e32 v100, v214, v100
	v_exp_f32_e32 v120, v160
	v_exp_f32_e32 v121, v161
	v_exp_f32_e32 v122, v134
	v_exp_f32_e32 v123, v135
	s_waitcnt lgkmcnt(12)
	v_mfma_f32_32x32x16_bf16 v[64:79], v[154:157], v[96:99], v[64:79]
	v_add_f32_e32 v96, v211, v100
	v_add_f32_e32 v96, v213, v96
	v_add_f32_e32 v96, v208, v96
	v_add_f32_e32 v96, v210, v96
	v_add_f32_e32 v96, v207, v96
	v_add_f32_e32 v96, v209, v96
	v_add_f32_e32 v96, v138, v96
	s_waitcnt lgkmcnt(7)
	v_mfma_f32_32x32x16_bf16 v[80:95], v[192:195], v[234:237], v[80:95]
	v_add_f32_e32 v96, v139, v96
	v_add_f32_e32 v96, v136, v96
	v_add_f32_e32 v96, v137, v96
	v_add_f32_e32 v96, v132, v96
	v_add_f32_e32 v96, v118, v96
	v_add_f32_e32 v96, v119, v96
	v_add_f32_e32 v96, v130, v96
	v_mfma_f32_32x32x16_bf16 v[64:79], v[226:229], v[234:237], v[64:79]
	v_add_f32_e32 v96, v128, v96
	v_add_f32_e32 v96, v129, v96
	v_add_f32_e32 v96, v131, v96
	v_add_f32_e32 v96, v133, v96
	v_add_f32_e32 v96, v120, v96
	v_add_f32_e32 v96, v121, v96
	v_add_f32_e32 v96, v122, v96
	s_waitcnt lgkmcnt(6)
	v_mfma_f32_32x32x16_bf16 v[80:95], v[112:115], v[238:241], v[80:95]
	v_add_f32_e32 v96, v123, v96
	v_mov_b32_e32 v97, v96
	s_nop 1
	v_permlane32_swap_b32_e32 v96, v97
	v_cvt_pk_bf16_f32 v100, v222, v224
	v_cvt_pk_bf16_f32 v101, v220, v223
	v_cvt_pk_bf16_f32 v102, v219, v221
	v_mfma_f32_32x32x16_bf16 v[64:79], v[230:233], v[238:241], v[64:79]
	v_cvt_pk_bf16_f32 v103, v217, v218
	v_cvt_pk_bf16_f32 v112, v212, v214
	v_cvt_pk_bf16_f32 v113, v211, v213
	v_cvt_pk_bf16_f32 v114, v208, v210
	v_cvt_pk_bf16_f32 v115, v207, v209
	v_cvt_pk_bf16_f32 v118, v132, v118
	v_cvt_pk_bf16_f32 v119, v119, v130
	s_waitcnt lgkmcnt(1)
	v_mfma_f32_32x32x16_bf16 v[80:95], v[242:245], v[104:107], v[80:95]
	v_permlane32_swap_b32_e32 v100, v102
	v_permlane32_swap_b32_e32 v101, v103
	v_permlane32_swap_b32_e32 v112, v114
	v_permlane32_swap_b32_e32 v113, v115
	v_mfma_f32_32x32x16_bf16 v[64:79], v[246:249], v[104:107], v[64:79]
	v_cvt_pk_bf16_f32 v104, v128, v129
	v_cvt_pk_bf16_f32 v105, v131, v133
	v_cvt_pk_bf16_f32 v106, v120, v121
	v_cvt_pk_bf16_f32 v107, v122, v123
	v_permlane32_swap_b32_e32 v116, v118
	v_permlane32_swap_b32_e32 v117, v119
	s_waitcnt lgkmcnt(0)
	v_mfma_f32_32x32x16_bf16 v[80:95], v[250:253], v[108:111], v[80:95]
	v_permlane32_swap_b32_e32 v104, v106
	v_permlane32_swap_b32_e32 v105, v107
	v_mfma_f32_32x32x16_bf16 v[64:79], v[200:203], v[108:111], v[64:79]
	ds_read_b64_tr_b16 v[108:109], v167 offset:0
	ds_read_b64_tr_b16 v[110:111], v167 offset:0x800
	ds_read_b64_tr_b16 v[120:121], v167 offset:0x1000
	ds_read_b64_tr_b16 v[122:123], v167 offset:0x1800
	ds_read_b64_tr_b16 v[124:125], v167 offset:0x2000
	ds_read_b64_tr_b16 v[126:127], v167 offset:0x2800
	ds_read_b64_tr_b16 v[128:129], v167 offset:0x3000
	ds_read_b64_tr_b16 v[130:131], v167 offset:0x3800
	s_nop 8
	v_max_f32_e32 v98, v81, v81
	v_max_f32_e32 v99, v80, v80
	v_max_f32_e32 v98, v99, v98
	v_max3_f32 v98, v98, v82, v83
	v_max3_f32 v98, v98, v84, v85
	v_max3_f32 v98, v98, v86, v87
	v_max3_f32 v98, v98, v88, v89
	v_max3_f32 v98, v98, v90, v91
	v_max3_f32 v98, v98, v92, v93
	v_max3_f32 v98, v98, v94, v95
	s_waitcnt lgkmcnt(0)
	v_mfma_f32_32x32x16_bf16 v[16:31], v[100:103], v[108:111], v[16:31]
	ds_read_b64_tr_b16 v[108:109], v167 offset:0x200
	ds_read_b64_tr_b16 v[110:111], v167 offset:0xa00
	v_mfma_f32_32x32x16_bf16 v[16:31], v[112:115], v[120:123], v[16:31]
	ds_read_b64_tr_b16 v[120:121], v167 offset:0x1200
	ds_read_b64_tr_b16 v[122:123], v167 offset:0x1a00
	v_mfma_f32_32x32x16_bf16 v[16:31], v[116:119], v[124:127], v[16:31]
	ds_read_b64_tr_b16 v[124:125], v167 offset:0x2200
	ds_read_b64_tr_b16 v[126:127], v167 offset:0x2a00
	ds_read_b64_tr_b16 v[132:133], v167 offset:0x3200
	ds_read_b64_tr_b16 v[134:135], v167 offset:0x3a00
	v_mfma_f32_32x32x16_bf16 v[16:31], v[104:107], v[128:131], v[16:31]
	v_max3_f32 v98, v98, v64, v65
	v_max3_f32 v98, v98, v66, v67
	v_max3_f32 v98, v98, v68, v69
	v_max3_f32 v98, v98, v70, v71
	v_max3_f32 v98, v98, v72, v73
	v_max3_f32 v98, v98, v74, v75
	v_max3_f32 v98, v98, v76, v77
	v_max3_f32 v98, v98, v78, v79
	v_mov_b32_e32 v99, v98
	s_nop 1
	v_permlane32_swap_b32_e32 v98, v99
	v_max_f32_e32 v99, v99, v99
	v_max_f32_e32 v98, v98, v98
	v_max_f32_e32 v98, v98, v99
	v_max_f32_e32 v99, v198, v198
	v_max_f32_e32 v99, v99, v98
	v_sub_f32_e32 v128, v98, v198
	v_sub_f32_e32 v98, v198, v99
	v_mul_f32_e32 v98, 0x3dd53b94, v98
	v_exp_f32_e32 v98, v98
	v_cmp_ge_f32_e32 vcc, s48, v128
	s_cmp_eq_u64 vcc, exec
	s_cselect_b64 s[6:7], -1, 0
	v_cndmask_b32_e64 v98, v98, 1.0, s[6:7]
	s_waitcnt lgkmcnt(0)
	v_mfma_f32_32x32x16_bf16 v[32:47], v[100:103], v[108:111], v[32:47]
	ds_read_b64_tr_b16 v[108:109], v167 offset:0x400
	ds_read_b64_tr_b16 v[110:111], v167 offset:0xc00
	v_mfma_f32_32x32x16_bf16 v[32:47], v[112:115], v[120:123], v[32:47]
	ds_read_b64_tr_b16 v[120:121], v167 offset:0x1400
	ds_read_b64_tr_b16 v[122:123], v167 offset:0x1c00
	v_mfma_f32_32x32x16_bf16 v[32:47], v[116:119], v[124:127], v[32:47]
	ds_read_b64_tr_b16 v[124:125], v167 offset:0x2400
	ds_read_b64_tr_b16 v[126:127], v167 offset:0x2c00
	ds_read_b64_tr_b16 v[128:129], v167 offset:0x3400
	ds_read_b64_tr_b16 v[130:131], v167 offset:0x3c00
	v_mfma_f32_32x32x16_bf16 v[32:47], v[104:107], v[132:135], v[32:47]
	s_waitcnt lgkmcnt(0)
	v_mfma_f32_32x32x16_bf16 v[0:15], v[100:103], v[108:111], v[0:15]
	ds_read_b64_tr_b16 v[108:109], v167 offset:0x600
	ds_read_b64_tr_b16 v[110:111], v167 offset:0xe00
	v_mfma_f32_32x32x16_bf16 v[0:15], v[112:115], v[120:123], v[0:15]
	ds_read_b64_tr_b16 v[120:121], v167 offset:0x1600
	ds_read_b64_tr_b16 v[122:123], v167 offset:0x1e00
	v_mfma_f32_32x32x16_bf16 v[0:15], v[116:119], v[124:127], v[0:15]
	ds_read_b64_tr_b16 v[124:125], v167 offset:0x2600
	ds_read_b64_tr_b16 v[126:127], v167 offset:0x2e00
	ds_read_b64_tr_b16 v[132:133], v167 offset:0x3600
	ds_read_b64_tr_b16 v[134:135], v167 offset:0x3e00
	v_mfma_f32_32x32x16_bf16 v[0:15], v[104:107], v[128:131], v[0:15]
	s_waitcnt lgkmcnt(0)
	v_mfma_f32_32x32x16_bf16 v[48:63], v[100:103], v[108:111], v[48:63]
	v_cmp_gt_f32_e32 vcc, 1.0, v98
	s_waitcnt vmcnt(0)
	s_barrier
	v_mfma_f32_32x32x16_bf16 v[48:63], v[112:115], v[120:123], v[48:63]
	v_mfma_f32_32x32x16_bf16 v[48:63], v[116:119], v[124:127], v[48:63]
	v_mfma_f32_32x32x16_bf16 v[48:63], v[104:107], v[132:135], v[48:63]
	s_cbranch_vccz .LBB0_771
	s_and_saveexec_b64 s[8:9], s[4:5]
	ds_write_b32 v189, v98 offset:128
	s_or_b64 exec, exec, s[8:9]
	s_waitcnt lgkmcnt(0)
	v_add_u32_e32 v112, s62, v169
	ds_read_b128 v[100:103], v112 offset:224
	ds_read_b128 v[104:107], v112 offset:192
	ds_read_b128 v[108:111], v112 offset:160
	ds_read_b128 v[112:115], v112 offset:128
	s_waitcnt lgkmcnt(3)
	v_pk_mul_f32 v[28:29], v[28:29], v[100:101]
	s_waitcnt lgkmcnt(2)
	v_pk_mul_f32 v[24:25], v[24:25], v[104:105]
	s_waitcnt lgkmcnt(1)
	v_pk_mul_f32 v[20:21], v[20:21], v[108:109]
	v_pk_mul_f32 v[30:31], v[30:31], v[102:103]
	v_pk_mul_f32 v[26:27], v[26:27], v[106:107]
	v_pk_mul_f32 v[22:23], v[22:23], v[110:111]
	s_waitcnt lgkmcnt(0)
	v_pk_mul_f32 v[18:19], v[18:19], v[114:115]
	v_pk_mul_f32 v[16:17], v[16:17], v[112:113]
	v_pk_mul_f32 v[44:45], v[44:45], v[100:101]
	v_pk_mul_f32 v[40:41], v[40:41], v[104:105]
	v_pk_mul_f32 v[36:37], v[36:37], v[108:109]
	v_pk_mul_f32 v[46:47], v[46:47], v[102:103]
	v_pk_mul_f32 v[42:43], v[42:43], v[106:107]
	v_pk_mul_f32 v[38:39], v[38:39], v[110:111]
	v_pk_mul_f32 v[34:35], v[34:35], v[114:115]
	v_pk_mul_f32 v[32:33], v[32:33], v[112:113]
	v_pk_mul_f32 v[12:13], v[12:13], v[100:101]
	v_pk_mul_f32 v[8:9], v[8:9], v[104:105]
	v_pk_mul_f32 v[4:5], v[4:5], v[108:109]
	v_pk_mul_f32 v[14:15], v[14:15], v[102:103]
	v_pk_mul_f32 v[10:11], v[10:11], v[106:107]
	v_pk_mul_f32 v[6:7], v[6:7], v[110:111]
	v_pk_mul_f32 v[2:3], v[2:3], v[114:115]
	v_pk_mul_f32 v[0:1], v[0:1], v[112:113]
	v_pk_mul_f32 v[60:61], v[60:61], v[100:101]
	v_pk_mul_f32 v[56:57], v[56:57], v[104:105]
	v_pk_mul_f32 v[52:53], v[52:53], v[108:109]
	v_pk_mul_f32 v[62:63], v[62:63], v[102:103]
	v_pk_mul_f32 v[58:59], v[58:59], v[106:107]
	v_pk_mul_f32 v[54:55], v[54:55], v[110:111]
	v_pk_mul_f32 v[50:51], v[50:51], v[114:115]
	v_pk_mul_f32 v[48:49], v[48:49], v[112:113]

.LBB0_2011:
	s_ashr_i32 s6, s11, 3
	s_lshl_b32 s60, s6, 8
	s_lshl_b32 s61, s6, 12
	s_lshl_b32 s6, s10, 8
	s_and_b32 s6, s6, 0xf00
	s_or_b32 s28, s61, s6
	s_add_i32 s8, s60, 0x4000
	s_and_b32 s12, s11, 7
	s_ashr_i32 s29, s28, 31
	s_mul_i32 s7, s28, 0xc00
	s_mul_hi_i32 s6, s28, 0xc00
	s_add_u32 s7, s35, s7
	s_addc_u32 s6, s36, s6
	s_mul_i32 s13, s12, 0x180
	s_add_u32 s10, s7, s13
	s_addc_u32 s11, s6, 0
	s_add_u32 s6, s37, s13
	s_addc_u32 s7, s38, 0
	s_lshl_b32 s59, s12, 7
	s_lshl_b32 s12, s12, 8
	s_add_u32 s30, s39, s12
	v_readfirstlane_b32 s62, v254
	s_addc_u32 s31, s40, 0
	s_ashr_i32 s12, s62, 6
	s_lshl_b32 s82, s12, 10
	s_mov_b32 s72, s6
	s_and_b32 s73, s7, 0xffff
	s_mov_b32 s74, 0x7ffffff0
	s_mov_b32 s75, 0x20000
	s_mov_b32 s76, s30
	s_and_b32 s77, s31, 0xffff
	s_mov_b32 s78, 0x7ffffff0
	s_mov_b32 s79, 0x20000
	v_lshl_add_u64 v[26:27], s[8:9], 0, v[142:143]
	v_lshl_add_u64 v[28:29], v[146:147], 0, s[8:9]
	v_lshl_or_b32 v2, s12, 5, v188
	v_mov_b64_e32 v[0:1], s[10:11]
	v_lshlrev_b64 v[16:17], 11, v[26:27]
	v_lshlrev_b64 v[18:19], 11, v[28:29]
	v_mad_i64_i32 v[0:1], s[10:11], v2, s44, v[0:1]
	v_lshl_add_u64 v[16:17], s[30:31], 0, v[16:17]
	v_lshl_add_u64 v[18:19], s[30:31], 0, v[18:19]
	v_lshl_add_u64 v[38:39], v[0:1], 0, v[148:149]
	v_lshl_add_u64 v[16:17], v[16:17], 0, v[150:151]
	v_lshl_add_u64 v[22:23], v[18:19], 0, v[150:151]
	global_load_dwordx4 v[0:3], v[38:39], off offset:256
	global_load_dwordx4 v[4:7], v[38:39], off offset:288
	global_load_dwordx4 v[8:11], v[38:39], off offset:320
	global_load_dwordx4 v[12:15], v[38:39], off offset:352
	global_load_dwordx4 v[18:21], v[16:17], off
	s_nop 0
	global_load_dwordx4 v[22:25], v[22:23], off
	v_mov_b64_e32 v[16:17], s[6:7]
	v_mad_u64_u32 v[30:31], s[10:11], v26, s44, v[16:17]
	v_mad_i32_i24 v31, v27, s44, v31
	v_lshl_add_u64 v[26:27], v[30:31], 0, v[150:151]
	v_mad_u64_u32 v[30:31], s[10:11], v28, s44, v[16:17]
	v_mad_i32_i24 v31, v29, s44, v31
	v_lshl_add_u64 v[30:31], v[30:31], 0, v[150:151]
	v_lshl_add_u64 v[34:35], s[8:9], 0, v[144:145]
	global_load_dwordx4 v[26:29], v[26:27], off
	s_nop 0
	global_load_dwordx4 v[30:33], v[30:31], off
	v_mad_u64_u32 v[36:37], s[10:11], v34, s44, v[16:17]
	v_mad_i32_i24 v37, v35, s44, v37
	v_lshl_add_u64 v[34:35], v[36:37], 0, v[152:153]
	global_load_dwordx4 v[34:37], v[34:35], off offset:256
	s_nop 0
	global_load_dwordx4 v[124:127], v[38:39], off
	global_load_dwordx4 v[120:123], v[38:39], off offset:32
	global_load_dwordx4 v[116:119], v[38:39], off offset:64
	global_load_dwordx4 v[112:115], v[38:39], off offset:96
	global_load_dwordx4 v[108:111], v[38:39], off offset:128
	global_load_dwordx4 v[104:107], v[38:39], off offset:160
	global_load_dwordx4 v[100:103], v[38:39], off offset:192
	global_load_dwordx4 v[96:99], v[38:39], off offset:224
	s_lshl_b32 s8, s12, 12
	v_add_u32_e32 v190, s8, v166
	v_add_u32_e32 v191, s45, v170
	v_add_u32_e32 v192, s45, v171
	v_add_u32_e32 v193, s45, v172
	v_add_u32_e32 v194, s45, v173
	s_mov_b32 s8, s9
	s_mov_b32 s10, s9
	s_mov_b32 s11, s9
	s_mov_b32 s12, s9
	s_mov_b32 s13, s9
	s_mov_b32 s14, s9
	s_mov_b32 s15, s9
	s_mov_b32 s16, s9
	s_mov_b32 s17, s9
	s_mov_b32 s18, s9
	s_mov_b32 s19, s9
	s_mov_b32 s20, s9
	s_mov_b32 s21, s9
	s_mov_b32 s22, s9
	s_mov_b32 s23, s9
	v_add_u32_e32 v195, 0, v168
	v_mov_b32_e32 v140, 0
	v_add_u32_e32 v196, 0x12000, v195
	v_lshrrev_b32_e32 v156, 4, v254
	v_and_b32_e32 v157, 7, v156
	v_and_b32_e32 v159, 15, v254
	v_xor_b32_e32 v157, v157, v159
	v_lshlrev_b32_e32 v157, 4, v157
	v_mad_u32_u24 v154, v156, s44, v157
	v_lshrrev_b32_e32 v156, 3, v254
	v_and_b32_e32 v157, 7, v156
	v_and_b32_e32 v159, 7, v254
	v_xor_b32_e32 v157, v157, v159
	v_lshlrev_b32_e32 v157, 4, v157
	v_add_u32_e32 v157, 0x100, v157
	v_mad_u32_u24 v155, v156, s44, v157
	v_and_b32_e32 v158, 3, v254
	v_lshlrev_b32_e32 v158, 4, v158
	v_bfe_u32 v156, v254, 5, 2
	v_lshl_or_b32 v158, v156, 6, v158
	v_bfe_u32 v156, v254, 2, 2
	v_lshl_or_b32 v158, v156, 11, v158
	v_bfe_u32 v156, v254, 7, 1
	v_lshl_or_b32 v158, v156, 13, v158
	v_bfe_u32 v156, v254, 4, 1
	v_lshl_or_b32 v158, v156, 14, v158
	v_bfe_u32 v156, v254, 8, 1
	v_lshl_or_b32 v158, v156, 15, v158
	s_waitcnt vmcnt(16)
	ds_write_b128 v190, v[0:3]
	s_waitcnt vmcnt(15)
	ds_write_b128 v190, v[4:7] offset:1024
	s_waitcnt vmcnt(14)
	ds_write_b128 v190, v[8:11] offset:2048
	s_waitcnt vmcnt(13)
	ds_write_b128 v190, v[12:15] offset:3072
	s_waitcnt vmcnt(0)
	s_waitcnt vmcnt(12)
	ds_write_b128 v175, v[18:21]
	s_waitcnt vmcnt(11)
	ds_write_b128 v176, v[22:25]
	s_waitcnt vmcnt(10)
	ds_write_b128 v177, v[26:29] offset:32768
	s_waitcnt vmcnt(9)
	ds_write_b128 v178, v[30:33] offset:32768
	s_waitcnt vmcnt(8)
	ds_write_b128 v179, v[34:37]
	s_waitcnt lgkmcnt(0)
	s_barrier
	ds_read_b128 v[0:3], v180 offset:32768
	ds_read_b128 v[4:7], v180 offset:40960
	s_waitcnt vmcnt(7) lgkmcnt(1)
	v_mfma_f32_32x32x16_bf16 v[48:63], v[0:3], v[124:127], 0
	s_waitcnt lgkmcnt(0)
	v_mfma_f32_32x32x16_bf16 v[64:79], v[4:7], v[124:127], 0
	ds_read_b128 v[0:3], v181 offset:32768
	ds_read_b128 v[4:7], v181 offset:40960
	s_waitcnt vmcnt(6) lgkmcnt(1)
	v_mfma_f32_32x32x16_bf16 v[48:63], v[0:3], v[120:123], v[48:63]
	s_waitcnt lgkmcnt(0)
	v_mfma_f32_32x32x16_bf16 v[64:79], v[4:7], v[120:123], v[64:79]
	ds_read_b128 v[0:3], v182 offset:32768
	ds_read_b128 v[4:7], v182 offset:40960
	s_waitcnt vmcnt(5) lgkmcnt(1)
	v_mfma_f32_32x32x16_bf16 v[48:63], v[0:3], v[116:119], v[48:63]
	s_waitcnt lgkmcnt(0)
	v_mfma_f32_32x32x16_bf16 v[64:79], v[4:7], v[116:119], v[64:79]
	ds_read_b128 v[0:3], v183 offset:32768
	ds_read_b128 v[4:7], v183 offset:40960
	s_waitcnt vmcnt(4) lgkmcnt(1)
	v_mfma_f32_32x32x16_bf16 v[48:63], v[0:3], v[112:115], v[48:63]
	s_waitcnt lgkmcnt(0)
	v_mfma_f32_32x32x16_bf16 v[64:79], v[4:7], v[112:115], v[64:79]
	ds_read_b128 v[0:3], v184 offset:32768
	ds_read_b128 v[4:7], v184 offset:40960
	s_waitcnt vmcnt(3) lgkmcnt(1)
	v_mfma_f32_32x32x16_bf16 v[48:63], v[0:3], v[108:111], v[48:63]
	s_waitcnt lgkmcnt(0)
	v_mfma_f32_32x32x16_bf16 v[64:79], v[4:7], v[108:111], v[64:79]
	ds_read_b128 v[0:3], v185 offset:32768
	ds_read_b128 v[4:7], v185 offset:40960
	s_waitcnt vmcnt(2) lgkmcnt(1)
	v_mfma_f32_32x32x16_bf16 v[48:63], v[0:3], v[104:107], v[48:63]
	s_waitcnt lgkmcnt(0)
	v_mfma_f32_32x32x16_bf16 v[64:79], v[4:7], v[104:107], v[64:79]
	ds_read_b128 v[0:3], v186 offset:32768
	ds_read_b128 v[4:7], v186 offset:40960
	s_waitcnt vmcnt(1) lgkmcnt(1)
	v_mfma_f32_32x32x16_bf16 v[48:63], v[0:3], v[100:103], v[48:63]
	s_waitcnt lgkmcnt(0)
	v_mfma_f32_32x32x16_bf16 v[64:79], v[4:7], v[100:103], v[64:79]
	ds_read_b128 v[0:3], v187 offset:32768
	ds_read_b128 v[4:7], v187 offset:40960
	s_waitcnt vmcnt(0) lgkmcnt(1)
	v_mfma_f32_32x32x16_bf16 v[48:63], v[0:3], v[96:99], v[48:63]
	s_waitcnt lgkmcnt(0)
	v_mfma_f32_32x32x16_bf16 v[64:79], v[4:7], v[96:99], v[64:79]
	ds_read_b128 v[0:3], v191
	ds_read_b128 v[4:7], v190
	ds_read_b128 v[8:11], v191 offset:4096
	ds_read_b128 v[12:15], v190 offset:1024
	s_waitcnt lgkmcnt(2)
	v_mfma_f32_32x32x16_bf16 v[48:63], v[0:3], v[4:7], v[48:63]
	s_waitcnt lgkmcnt(1)
	v_mfma_f32_32x32x16_bf16 v[64:79], v[8:11], v[4:7], v[64:79]
	ds_read_b128 v[0:3], v192
	ds_read_b128 v[4:7], v192 offset:4096
	s_waitcnt lgkmcnt(1)
	v_mfma_f32_32x32x16_bf16 v[48:63], v[0:3], v[12:15], v[48:63]
	s_waitcnt lgkmcnt(0)
	v_mfma_f32_32x32x16_bf16 v[64:79], v[4:7], v[12:15], v[64:79]
	ds_read_b128 v[0:3], v193
	ds_read_b128 v[4:7], v190 offset:2048
	ds_read_b128 v[8:11], v193 offset:4096
	ds_read_b128 v[18:21], v190 offset:3072
	ds_read_b128 v[22:25], v194 offset:4096
	s_waitcnt lgkmcnt(3)
	v_mfma_f32_32x32x16_bf16 v[48:63], v[0:3], v[4:7], v[48:63]
	ds_read_b128 v[0:3], v194
	s_waitcnt lgkmcnt(3)
	v_mfma_f32_32x32x16_bf16 v[64:79], v[8:11], v[4:7], v[64:79]
	s_waitcnt lgkmcnt(0)
	v_mfma_f32_32x32x16_bf16 v[48:63], v[0:3], v[18:21], v[48:63]
	v_mov_b64_e32 v[0:1], s[8:9]
	v_mov_b64_e32 v[2:3], s[10:11]
	v_mov_b64_e32 v[4:5], s[12:13]
	v_mov_b64_e32 v[6:7], s[14:15]
	v_mov_b64_e32 v[8:9], s[16:17]
	v_mov_b64_e32 v[10:11], s[18:19]
	v_mov_b64_e32 v[12:13], s[20:21]
	v_mfma_f32_32x32x16_bf16 v[64:79], v[22:25], v[18:21], v[64:79]
	s_nop 3
	v_max_f32_e32 v18, v49, v49
	v_max_f32_e32 v19, v48, v48
	v_max_f32_e32 v18, v19, v18
	v_max3_f32 v18, v18, v50, v51
	v_max3_f32 v18, v18, v52, v53
	v_max3_f32 v18, v18, v54, v55
	v_max3_f32 v18, v18, v56, v57
	v_max3_f32 v18, v18, v58, v59
	v_max3_f32 v18, v18, v60, v61
	v_max3_f32 v18, v18, v62, v63
	v_max3_f32 v18, v18, v64, v65
	v_max3_f32 v18, v18, v66, v67
	v_max3_f32 v18, v18, v68, v69
	v_max3_f32 v18, v18, v70, v71
	v_max3_f32 v18, v18, v72, v73
	v_max3_f32 v18, v18, v74, v75
	v_max3_f32 v18, v18, v76, v77
	v_max3_f32 v18, v18, v78, v79
	v_mov_b32_e32 v19, v18
	s_nop 1
	v_permlane32_swap_b32_e32 v18, v19
	v_mov_b64_e32 v[14:15], s[22:23]
	s_and_b32 s8, s62, 0x3fffffc0
	v_max_f32_e32 v19, v19, v19
	v_max_f32_e32 v18, v18, v18
	s_lshl_b32 s8, s8, 2
	v_max_f32_e32 v18, v18, v19
	s_add_i32 s12, s8, 0
	v_add_f32_e32 v19, 0x7149f2ca, v18
	s_add_i32 s12, s12, 0x14000
	v_cmp_ge_f32_e32 vcc, s46, v19
	s_cmp_eq_u64 vcc, exec
	s_cselect_b64 vcc, -1, 0
	s_add_i32 s8, s60, 0x4040
	v_max_f32_e32 v128, 0xf149f2ca, v18
	v_lshl_add_u64 v[18:19], s[8:9], 0, v[142:143]
	v_lshl_add_u64 v[20:21], v[146:147], 0, s[8:9]
	v_lshl_add_u64 v[22:23], s[8:9], 0, v[144:145]
	v_lshlrev_b64 v[24:25], 11, v[18:19]
	v_lshlrev_b64 v[26:27], 11, v[20:21]
	v_mad_u64_u32 v[28:29], s[10:11], v18, s44, v[16:17]
	v_mad_u64_u32 v[30:31], s[10:11], v20, s44, v[16:17]
	v_mad_u64_u32 v[16:17], s[10:11], v22, s44, v[16:17]
	v_lshl_add_u64 v[24:25], s[30:31], 0, v[24:25]
	v_lshl_add_u64 v[26:27], s[30:31], 0, v[26:27]
	v_mad_i32_i24 v29, v19, s44, v29
	v_mad_i32_i24 v31, v21, s44, v31
	v_mad_i32_i24 v17, v23, s44, v17
	v_lshl_add_u64 v[18:19], v[24:25], 0, v[150:151]
	v_lshl_add_u64 v[20:21], v[26:27], 0, v[150:151]
	v_lshl_add_u64 v[22:23], v[28:29], 0, v[150:151]
	v_lshl_add_u64 v[24:25], v[30:31], 0, v[150:151]
	v_lshl_add_u64 v[16:17], v[16:17], 0, v[152:153]
	global_load_dwordx4 v[80:83], v[18:19], off
	global_load_dwordx4 v[84:87], v[20:21], off
	global_load_dwordx4 v[88:91], v[22:23], off
	global_load_dwordx4 v[92:95], v[24:25], off
	global_load_dwordx4 v[200:203], v[16:17], off offset:256
	v_sub_f32_e32 v129, 0xf149f2ca, v128
	v_mul_f32_e32 v129, 0x3dd53b94, v129
	v_exp_f32_e32 v164, v129
	v_mov_b32_e32 v129, 0xf149f2ca
	v_cndmask_b32_e32 v198, v128, v129, vcc
	v_mul_f32_e32 v138, 0xbdd53b94, v198
	v_mov_b32_e32 v165, v138
	v_fmamk_f32 v48, v48, 0x3dd53b94, v138
	v_fmamk_f32 v49, v49, 0x3dd53b94, v138
	v_fmamk_f32 v50, v50, 0x3dd53b94, v138
	v_fmamk_f32 v51, v51, 0x3dd53b94, v138
	v_fmamk_f32 v52, v52, 0x3dd53b94, v138
	v_fmamk_f32 v53, v53, 0x3dd53b94, v138
	v_fmamk_f32 v54, v54, 0x3dd53b94, v138
	v_fmamk_f32 v55, v55, 0x3dd53b94, v138
	v_fmamk_f32 v56, v56, 0x3dd53b94, v138
	v_fmamk_f32 v57, v57, 0x3dd53b94, v138
	v_fmamk_f32 v58, v58, 0x3dd53b94, v138
	v_fmamk_f32 v59, v59, 0x3dd53b94, v138
	v_fmamk_f32 v60, v60, 0x3dd53b94, v138
	v_fmamk_f32 v61, v61, 0x3dd53b94, v138
	v_fmamk_f32 v62, v62, 0x3dd53b94, v138
	v_fmac_f32_e32 v165, 0x3dd53b94, v63
	v_exp_f32_e32 v222, v48
	v_exp_f32_e32 v224, v49
	v_exp_f32_e32 v220, v50
	v_exp_f32_e32 v223, v51
	v_exp_f32_e32 v219, v52
	v_exp_f32_e32 v221, v53
	v_exp_f32_e32 v217, v54
	v_exp_f32_e32 v218, v55
	v_exp_f32_e32 v212, v56
	v_exp_f32_e32 v214, v57
	v_exp_f32_e32 v211, v58
	v_exp_f32_e32 v213, v59
	v_exp_f32_e32 v208, v60
	v_exp_f32_e32 v210, v61
	v_exp_f32_e32 v207, v62
	v_exp_f32_e32 v209, v165
	s_waitcnt vmcnt(0)
	v_mov_b64_e32 v[46:47], v[14:15]
	v_mov_b64_e32 v[30:31], v[14:15]
	v_mov_b64_e32 v[62:63], v[14:15]
	s_mov_b32 s8, -1
	v_mov_b64_e32 v[44:45], v[12:13]
	v_mov_b64_e32 v[42:43], v[10:11]
	v_mov_b64_e32 v[40:41], v[8:9]
	v_mov_b64_e32 v[38:39], v[6:7]
	v_mov_b64_e32 v[36:37], v[4:5]
	v_mov_b64_e32 v[34:35], v[2:3]
	v_mov_b64_e32 v[32:33], v[0:1]
	v_mov_b64_e32 v[28:29], v[12:13]
	v_mov_b64_e32 v[26:27], v[10:11]
	v_mov_b64_e32 v[24:25], v[8:9]
	v_mov_b64_e32 v[22:23], v[6:7]
	v_mov_b64_e32 v[20:21], v[4:5]
	v_mov_b64_e32 v[18:19], v[2:3]
	v_mov_b64_e32 v[16:17], v[0:1]
	v_lshl_add_u32 v189, v188, 2, s12
	s_add_i32 s13, s60, 0x4080
	s_add_i32 s83, s60, 0x4040
	s_sub_i32 s14, s61, 64
	v_pk_fma_f32 v[134:135], v[78:79], s[26:27], v[138:139] op_sel_hi:[1,0,0]
	v_pk_fma_f32 v[160:161], v[76:77], s[26:27], v[138:139] op_sel_hi:[1,0,0]
	v_pk_fma_f32 v[162:163], v[74:75], s[26:27], v[138:139] op_sel_hi:[1,0,0]
	v_pk_fma_f32 v[128:129], v[72:73], s[26:27], v[138:139] op_sel_hi:[1,0,0]
	v_pk_fma_f32 v[130:131], v[70:71], s[26:27], v[138:139] op_sel_hi:[1,0,0]
	v_pk_fma_f32 v[132:133], v[68:69], s[26:27], v[138:139] op_sel_hi:[1,0,0]
	v_pk_fma_f32 v[136:137], v[66:67], s[26:27], v[138:139] op_sel_hi:[1,0,0]
	v_pk_fma_f32 v[138:139], v[64:65], s[26:27], v[138:139] op_sel_hi:[1,0,0]
	v_cndmask_b32_e64 v197, v164, 1.0, vcc
	v_mov_b64_e32 v[60:61], v[12:13]
	v_mov_b64_e32 v[58:59], v[10:11]
	v_mov_b64_e32 v[56:57], v[8:9]
	v_mov_b64_e32 v[54:55], v[6:7]
	v_mov_b64_e32 v[52:53], v[4:5]
	v_mov_b64_e32 v[50:51], v[2:3]
	v_mov_b64_e32 v[48:49], v[0:1]
	s_waitcnt vmcnt(4)
	ds_write_b128 v175, v[80:83] offset:16384
	s_waitcnt vmcnt(3)
	ds_write_b128 v176, v[84:87] offset:16384
	s_waitcnt vmcnt(2)
	ds_write_b128 v177, v[88:91] offset:49152
	s_waitcnt vmcnt(1)
	ds_write_b128 v178, v[92:95] offset:49152
	s_waitcnt vmcnt(0)
	ds_write_b128 v196, v[200:203]
	s_waitcnt lgkmcnt(0)
	s_barrier
	s_mov_b32 s80, s13
	s_mul_i32 s81, s80, 0xc00
	s_add_i32 s85, s82, 0x8000
	s_mov_b32 m0, s85
	s_add_i32 s85, s82, 0x10000
	buffer_load_dwordx4 v154, s[72:75], s81 offen lds
	s_mov_b32 m0, s85
	s_add_i32 s85, s82, 0xa000
	buffer_load_dwordx4 v155, s[72:75], s81 offen lds
	s_mov_b32 m0, s85
	s_add_i32 s81, s81, 0x18000
	buffer_load_dwordx4 v154, s[72:75], s81 offen lds
	s_lshl_b32 s81, s83, 11
	s_add_i32 s85, s82, 0x4000
	s_mov_b32 m0, s85
	s_add_i32 s85, s82, 0x6000
	buffer_load_dwordx4 v158, s[76:79], s81 offen lds
	s_mov_b32 m0, s85
	s_add_i32 s81, s81, 0x10000
	buffer_load_dwordx4 v158, s[76:79], s81 offen lds
	s_mov_b32 s84, s80
.LBB0_2012:
	s_add_i32 s8, s8, 2
	s_add_i32 s6, 0, 0x12000
	v_add_u32_e32 v199, s6, v170
	v_add_u32_e32 v204, s6, v171
	v_add_u32_e32 v205, s6, v172
	ds_read_b128 v[64:67], v180 offset:49152
	ds_read_b128 v[68:71], v180 offset:57344
	ds_read_b128 v[200:203], v181 offset:49152
	ds_read_b128 v[226:229], v181 offset:57344
	ds_read_b128 v[230:233], v182 offset:49152
	ds_read_b128 v[234:237], v182 offset:57344
	ds_read_b128 v[238:241], v183 offset:49152
	ds_read_b128 v[242:245], v183 offset:57344
	s_waitcnt lgkmcnt(7)
	v_mfma_f32_32x32x16_bf16 v[80:95], v[64:67], v[124:127], 0
	v_exp_f32_e32 v216, v128
	v_add_f32_e32 v128, 0, v222
	v_add_f32_e32 v128, v224, v128
	v_add_f32_e32 v128, v220, v128
	v_add_f32_e32 v128, v223, v128
	v_add_f32_e32 v128, v219, v128
	v_add_f32_e32 v128, v221, v128
	s_waitcnt lgkmcnt(6)
	v_mfma_f32_32x32x16_bf16 v[64:79], v[68:71], v[124:127], 0
	v_add_f32_e32 v128, v217, v128
	v_add_f32_e32 v128, v218, v128
	v_add_f32_e32 v128, v212, v128
	v_add_f32_e32 v128, v214, v128
	v_add_f32_e32 v128, v211, v128
	v_add_f32_e32 v128, v213, v128
	v_exp_f32_e32 v138, v138
	s_waitcnt lgkmcnt(5)
	v_mfma_f32_32x32x16_bf16 v[80:95], v[200:203], v[120:123], v[80:95]
	v_add_f32_e32 v128, v208, v128
	v_exp_f32_e32 v139, v139
	v_add_f32_e32 v128, v210, v128
	v_exp_f32_e32 v164, v136
	v_add_f32_e32 v128, v207, v128
	v_exp_f32_e32 v137, v137
	v_add_f32_e32 v128, v209, v128
	s_waitcnt lgkmcnt(4)
	v_mfma_f32_32x32x16_bf16 v[64:79], v[226:229], v[120:123], v[64:79]
	ds_read_b128 v[200:203], v184 offset:49152
	ds_read_b128 v[226:229], v184 offset:57344
	v_exp_f32_e32 v165, v132
	v_add_f32_e32 v128, v138, v128
	v_add_f32_e32 v128, v139, v128
	v_exp_f32_e32 v206, v130
	v_add_f32_e32 v128, v164, v128
	v_exp_f32_e32 v215, v131
	s_waitcnt lgkmcnt(5)
	v_mfma_f32_32x32x16_bf16 v[80:95], v[230:233], v[116:119], v[80:95]
	v_add_f32_e32 v128, v137, v128
	v_add_f32_e32 v128, v165, v128
	v_exp_f32_e32 v225, v129
	v_exp_f32_e32 v162, v162
	v_exp_f32_e32 v163, v163
	v_exp_f32_e32 v160, v160
	v_exp_f32_e32 v161, v161
	s_waitcnt lgkmcnt(4)
	v_mfma_f32_32x32x16_bf16 v[64:79], v[234:237], v[116:119], v[64:79]
	ds_read_b128 v[230:233], v185 offset:49152
	ds_read_b128 v[234:237], v185 offset:57344
	v_cvt_pk_bf16_f32 v129, v220, v223
	v_cvt_pk_bf16_f32 v130, v219, v221
	v_cvt_pk_bf16_f32 v131, v217, v218
	v_cvt_pk_bf16_f32 v132, v212, v214
	v_cvt_pk_bf16_f32 v136, v138, v139
	v_cvt_pk_bf16_f32 v137, v164, v137
	s_waitcnt lgkmcnt(5)
	v_mfma_f32_32x32x16_bf16 v[80:95], v[238:241], v[112:115], v[80:95]
	v_cvt_pk_bf16_f32 v139, v206, v215
	v_permlane32_swap_b32_e32 v129, v131
	s_nop 0
	v_permlane32_swap_b32_e32 v137, v139
	s_waitcnt lgkmcnt(4)
	v_mfma_f32_32x32x16_bf16 v[64:79], v[242:245], v[112:115], v[64:79]
	ds_read_b128 v[238:241], v186 offset:49152
	ds_read_b128 v[242:245], v186 offset:57344
	s_waitcnt lgkmcnt(5)
	v_mfma_f32_32x32x16_bf16 v[80:95], v[200:203], v[108:111], v[80:95]
	s_waitcnt lgkmcnt(4)
	v_mfma_f32_32x32x16_bf16 v[64:79], v[226:229], v[108:111], v[64:79]
	ds_read_b128 v[200:203], v187 offset:49152
	ds_read_b128 v[226:229], v187 offset:57344
	s_waitcnt lgkmcnt(5)
	v_mfma_f32_32x32x16_bf16 v[80:95], v[230:233], v[104:107], v[80:95]
	s_waitcnt lgkmcnt(4)
	v_mfma_f32_32x32x16_bf16 v[64:79], v[234:237], v[104:107], v[64:79]
	ds_read_b128 v[230:233], v199
	ds_read_b128 v[234:237], v199 offset:4096
	ds_read_b128 v[246:249], v190
	s_waitcnt lgkmcnt(6)
	v_mfma_f32_32x32x16_bf16 v[80:95], v[238:241], v[100:103], v[80:95]
	s_waitcnt lgkmcnt(5)
	v_mfma_f32_32x32x16_bf16 v[64:79], v[242:245], v[100:103], v[64:79]
	ds_read_b128 v[238:241], v204
	ds_read_b128 v[242:245], v204 offset:4096
	ds_read_b128 v[250:253], v190 offset:1024
	v_add_u32_e32 v204, s6, v173
	s_waitcnt lgkmcnt(7)
	v_mfma_f32_32x32x16_bf16 v[80:95], v[200:203], v[96:99], v[80:95]
	s_waitcnt lgkmcnt(6)
	v_mfma_f32_32x32x16_bf16 v[64:79], v[226:229], v[96:99], v[64:79]
	ds_read_b128 v[200:203], v205
	ds_read_b128 v[226:229], v205 offset:4096
	s_waitcnt lgkmcnt(5)
	v_mfma_f32_32x32x16_bf16 v[80:95], v[230:233], v[246:249], v[80:95]
	s_waitcnt lgkmcnt(5)
	v_mfma_f32_32x32x16_bf16 v[64:79], v[234:237], v[246:249], v[64:79]
	ds_read_b128 v[230:233], v204
	ds_read_b128 v[234:237], v204 offset:4096
	ds_read_b128 v[246:249], v190 offset:2048
	s_waitcnt lgkmcnt(5)
	v_mfma_f32_32x32x16_bf16 v[80:95], v[238:241], v[250:253], v[80:95]
	s_waitcnt lgkmcnt(5)
	v_mfma_f32_32x32x16_bf16 v[64:79], v[242:245], v[250:253], v[64:79]
	ds_read_b128 v[250:253], v190 offset:3072
	s_waitcnt lgkmcnt(1)
	v_mfma_f32_32x32x16_bf16 v[80:95], v[200:203], v[246:249], v[80:95]
	v_exp_f32_e32 v205, v133
	v_cvt_pk_bf16_f32 v133, v211, v213
	v_cvt_pk_bf16_f32 v138, v165, v205
	v_add_f32_e32 v128, v205, v128
	v_add_f32_e32 v128, v206, v128
	v_add_f32_e32 v128, v215, v128
	s_waitcnt lgkmcnt(1)
	v_mfma_f32_32x32x16_bf16 v[64:79], v[226:229], v[246:249], v[64:79]
	v_add_f32_e32 v128, v216, v128
	v_add_f32_e32 v128, v225, v128
	v_add_f32_e32 v128, v162, v128
	v_add_f32_e32 v128, v163, v128
	v_add_f32_e32 v128, v160, v128
	v_add_f32_e32 v128, v161, v128
	s_waitcnt lgkmcnt(0)
	v_mfma_f32_32x32x16_bf16 v[80:95], v[230:233], v[250:253], v[80:95]
	v_exp_f32_e32 v226, v134
	v_exp_f32_e32 v227, v135
	v_cvt_pk_bf16_f32 v134, v208, v210
	v_cvt_pk_bf16_f32 v135, v207, v209
	v_add_f32_e32 v128, v226, v128
	v_add_f32_e32 v203, v227, v128
	v_mov_b32_e32 v204, v203
	s_waitcnt lgkmcnt(0)
	v_mfma_f32_32x32x16_bf16 v[64:79], v[234:237], v[250:253], v[64:79]
	s_nop 0
	v_permlane32_swap_b32_e32 v203, v204
	v_cvt_pk_bf16_f32 v128, v222, v224
	v_cvt_pk_bf16_f32 v208, v216, v225
	v_cvt_pk_bf16_f32 v209, v162, v163
	v_cvt_pk_bf16_f32 v210, v160, v161
	v_cvt_pk_bf16_f32 v211, v226, v227
	v_permlane32_swap_b32_e32 v132, v134
	v_permlane32_swap_b32_e32 v128, v130
	v_permlane32_swap_b32_e32 v133, v135
	v_permlane32_swap_b32_e32 v136, v138
	v_permlane32_swap_b32_e32 v208, v210
	v_permlane32_swap_b32_e32 v209, v211
	ds_read_b64_tr_b16 v[160:161], v167 offset:0
	ds_read_b64_tr_b16 v[162:163], v167 offset:0x800
	ds_read_b64_tr_b16 v[232:233], v167 offset:0x1000
	ds_read_b64_tr_b16 v[234:235], v167 offset:0x1800
	ds_read_b64_tr_b16 v[236:237], v167 offset:0x2000
	ds_read_b64_tr_b16 v[238:239], v167 offset:0x2800
	ds_read_b64_tr_b16 v[240:241], v167 offset:0x3000
	ds_read_b64_tr_b16 v[242:243], v167 offset:0x3800
	v_max_f32_e32 v164, v81, v81
	v_max_f32_e32 v165, v80, v80
	v_max_f32_e32 v164, v165, v164
	v_max3_f32 v164, v164, v82, v83
	v_max3_f32 v164, v164, v84, v85
	v_max3_f32 v164, v164, v86, v87
	v_max3_f32 v164, v164, v88, v89
	v_max3_f32 v164, v164, v90, v91
	v_max3_f32 v164, v164, v92, v93
	v_max3_f32 v164, v164, v94, v95
	s_waitcnt lgkmcnt(0)
	v_mfma_f32_32x32x16_bf16 v[0:15], v[128:131], v[160:163], v[0:15]
	v_max3_f32 v160, v164, v64, v65
	v_max3_f32 v160, v160, v66, v67
	v_max3_f32 v160, v160, v68, v69
	v_mfma_f32_32x32x16_bf16 v[0:15], v[132:135], v[232:235], v[0:15]
	ds_read_b64_tr_b16 v[232:233], v167 offset:0x200
	ds_read_b64_tr_b16 v[234:235], v167 offset:0xa00
	v_max3_f32 v160, v160, v70, v71
	v_max3_f32 v160, v160, v72, v73
	v_max3_f32 v160, v160, v74, v75
	v_mfma_f32_32x32x16_bf16 v[0:15], v[136:139], v[236:239], v[0:15]
	ds_read_b64_tr_b16 v[236:237], v167 offset:0x1200
	ds_read_b64_tr_b16 v[238:239], v167 offset:0x1a00
	ds_read_b64_tr_b16 v[244:245], v167 offset:0x2200
	ds_read_b64_tr_b16 v[246:247], v167 offset:0x2a00
	ds_read_b64_tr_b16 v[248:249], v167 offset:0x3200
	ds_read_b64_tr_b16 v[250:251], v167 offset:0x3a00
	v_max3_f32 v160, v160, v76, v77
	v_max3_f32 v160, v160, v78, v79
	v_mov_b32_e32 v161, v160
	v_mfma_f32_32x32x16_bf16 v[0:15], v[208:211], v[240:243], v[0:15]
	v_max_f32_e32 v162, v198, v198
	v_permlane32_swap_b32_e32 v160, v161
	v_max_f32_e32 v161, v161, v161
	v_max_f32_e32 v160, v160, v160
	v_max_f32_e32 v160, v160, v161
	s_waitcnt lgkmcnt(0)
	v_mfma_f32_32x32x16_bf16 v[32:47], v[128:131], v[232:235], v[32:47]
	ds_read_b64_tr_b16 v[232:233], v167 offset:0x400
	ds_read_b64_tr_b16 v[234:235], v167 offset:0xc00
	v_sub_f32_e32 v161, v160, v198
	v_max_f32_e32 v160, v162, v160
	v_sub_f32_e32 v162, v198, v160
	v_mul_f32_e32 v162, 0x3dd53b94, v162
	v_exp_f32_e32 v162, v162
	v_mfma_f32_32x32x16_bf16 v[32:47], v[132:135], v[236:239], v[32:47]
	ds_read_b64_tr_b16 v[236:237], v167 offset:0x1400
	ds_read_b64_tr_b16 v[238:239], v167 offset:0x1c00
	ds_read_b64_tr_b16 v[240:241], v167 offset:0x2400
	ds_read_b64_tr_b16 v[242:243], v167 offset:0x2c00
	v_cmp_ge_f32_e32 vcc, s46, v161
	s_cmp_eq_u64 vcc, exec
	s_cselect_b64 s[6:7], -1, 0
	v_cndmask_b32_e64 v206, v162, 1.0, s[6:7]
	v_cndmask_b32_e64 v160, v160, v198, s[6:7]
	v_mul_f32_e32 v205, 0xbdd53b94, v160
	v_cmp_gt_f32_e32 vcc, 1.0, v206
	v_mfma_f32_32x32x16_bf16 v[32:47], v[136:139], v[244:247], v[32:47]
	ds_read_b64_tr_b16 v[244:245], v167 offset:0x3400
	ds_read_b64_tr_b16 v[246:247], v167 offset:0x3c00
	v_fmamk_f32 v87, v87, 0x3dd53b94, v205
	v_fmamk_f32 v80, v80, 0x3dd53b94, v205
	v_fmamk_f32 v81, v81, 0x3dd53b94, v205
	v_fmamk_f32 v82, v82, 0x3dd53b94, v205
	v_fmamk_f32 v83, v83, 0x3dd53b94, v205
	v_mfma_f32_32x32x16_bf16 v[32:47], v[208:211], v[248:251], v[32:47]
	v_fmamk_f32 v84, v84, 0x3dd53b94, v205
	v_fmamk_f32 v85, v85, 0x3dd53b94, v205
	v_fmamk_f32 v86, v86, 0x3dd53b94, v205
	v_fmamk_f32 v88, v88, 0x3dd53b94, v205
	v_fmamk_f32 v89, v89, 0x3dd53b94, v205
	s_waitcnt lgkmcnt(0)
	v_mfma_f32_32x32x16_bf16 v[16:31], v[128:131], v[232:235], v[16:31]
	ds_read_b64_tr_b16 v[232:233], v167 offset:0x600
	ds_read_b64_tr_b16 v[234:235], v167 offset:0xe00
	v_fmamk_f32 v90, v90, 0x3dd53b94, v205
	v_fmamk_f32 v91, v91, 0x3dd53b94, v205
	v_fmamk_f32 v92, v92, 0x3dd53b94, v205
	v_fmamk_f32 v93, v93, 0x3dd53b94, v205
	v_fmamk_f32 v94, v94, 0x3dd53b94, v205
	v_mfma_f32_32x32x16_bf16 v[16:31], v[132:135], v[236:239], v[16:31]
	ds_read_b64_tr_b16 v[236:237], v167 offset:0x1600
	ds_read_b64_tr_b16 v[238:239], v167 offset:0x1e00
	v_fmamk_f32 v95, v95, 0x3dd53b94, v205
	v_fmamk_f32 v215, v64, 0x3dd53b94, v205
	v_fmamk_f32 v216, v65, 0x3dd53b94, v205
	v_fmamk_f32 v217, v66, 0x3dd53b94, v205
	v_fmamk_f32 v218, v67, 0x3dd53b94, v205
	v_mfma_f32_32x32x16_bf16 v[16:31], v[136:139], v[240:243], v[16:31]
	ds_read_b64_tr_b16 v[240:241], v167 offset:0x2600
	ds_read_b64_tr_b16 v[242:243], v167 offset:0x2e00
	ds_read_b64_tr_b16 v[248:249], v167 offset:0x3600
	ds_read_b64_tr_b16 v[250:251], v167 offset:0x3e00
	v_fmamk_f32 v219, v68, 0x3dd53b94, v205
	v_fmamk_f32 v212, v73, 0x3dd53b94, v205
	v_fmamk_f32 v213, v74, 0x3dd53b94, v205
	v_fmamk_f32 v214, v75, 0x3dd53b94, v205
	v_mfma_f32_32x32x16_bf16 v[16:31], v[208:211], v[244:247], v[16:31]
	v_fmamk_f32 v207, v76, 0x3dd53b94, v205
	v_fmamk_f32 v220, v77, 0x3dd53b94, v205
	v_fmamk_f32 v221, v78, 0x3dd53b94, v205
	s_waitcnt vmcnt(0) lgkmcnt(0)
	s_barrier
	v_mfma_f32_32x32x16_bf16 v[48:63], v[128:131], v[232:235], v[48:63]
	s_add_i32 s80, s13, 64
	s_cmp_lt_u32 s8, 2
	s_cselect_b32 s80, s80, s14
	s_mul_i32 s81, s80, 0xc00
	s_add_i32 s85, s82, 0xc000
	s_mov_b32 m0, s85
	s_add_i32 s85, s82, 0x12000
	buffer_load_dwordx4 v154, s[72:75], s81 offen lds
	v_exp_f32_e32 v128, v80
	v_exp_f32_e32 v129, v82
	v_exp_f32_e32 v130, v84
	v_exp_f32_e32 v131, v86
	v_mfma_f32_32x32x16_bf16 v[48:63], v[132:135], v[236:239], v[48:63]
	s_mov_b32 m0, s85
	s_add_i32 s85, s82, 0xe000
	buffer_load_dwordx4 v155, s[72:75], s81 offen lds
	v_exp_f32_e32 v132, v88
	v_exp_f32_e32 v133, v90
	v_exp_f32_e32 v134, v92
	v_exp_f32_e32 v135, v94
	v_mfma_f32_32x32x16_bf16 v[48:63], v[136:139], v[240:243], v[48:63]
	s_mov_b32 m0, s85
	s_add_i32 s81, s81, 0x18000
	buffer_load_dwordx4 v154, s[72:75], s81 offen lds
	v_exp_f32_e32 v139, v89
	v_exp_f32_e32 v138, v91
	v_exp_f32_e32 v137, v93
	v_exp_f32_e32 v136, v95
	v_mfma_f32_32x32x16_bf16 v[48:63], v[208:211], v[248:251], v[48:63]
	s_lshl_b32 s81, s84, 11
	s_add_i32 s85, s82, 0x0
	s_mov_b32 m0, s85
	s_add_i32 s85, s82, 0x2000
	buffer_load_dwordx4 v158, s[76:79], s81 offen lds
	s_mov_b32 m0, s85
	s_add_i32 s81, s81, 0x10000
	buffer_load_dwordx4 v158, s[76:79], s81 offen lds
	s_mov_b32 s83, s80
	v_exp_f32_e32 v161, v87
	v_exp_f32_e32 v198, v81
	v_exp_f32_e32 v163, v83
	v_exp_f32_e32 v162, v85
	v_fmamk_f32 v208, v69, 0x3dd53b94, v205
	v_fmamk_f32 v209, v70, 0x3dd53b94, v205
	v_fmamk_f32 v210, v71, 0x3dd53b94, v205
	v_fmamk_f32 v211, v72, 0x3dd53b94, v205
	v_fmac_f32_e32 v205, 0x3dd53b94, v79
	s_cbranch_vccz .LBB0_2016
	s_and_saveexec_b64 s[10:11], s[4:5]
	ds_write_b32 v189, v206 offset:128
	s_or_b64 exec, exec, s[10:11]
	s_waitcnt lgkmcnt(0)
	v_add_u32_e32 v248, s12, v169
	ds_read_b128 v[232:235], v248 offset:224
	ds_read_b128 v[236:239], v248 offset:192
	ds_read_b128 v[240:243], v248 offset:160
	ds_read_b128 v[244:247], v248 offset:128
	s_waitcnt lgkmcnt(3)
	v_pk_mul_f32 v[12:13], v[12:13], v[232:233]
	s_waitcnt lgkmcnt(2)
	v_pk_mul_f32 v[8:9], v[8:9], v[236:237]
	s_waitcnt lgkmcnt(1)
	v_pk_mul_f32 v[4:5], v[4:5], v[240:241]
	v_pk_mul_f32 v[14:15], v[14:15], v[234:235]
	v_pk_mul_f32 v[10:11], v[10:11], v[238:239]
	v_pk_mul_f32 v[6:7], v[6:7], v[242:243]
	s_waitcnt lgkmcnt(0)
	v_pk_mul_f32 v[2:3], v[2:3], v[246:247]
	v_pk_mul_f32 v[0:1], v[0:1], v[244:245]
	v_pk_mul_f32 v[44:45], v[44:45], v[232:233]
	v_pk_mul_f32 v[40:41], v[40:41], v[236:237]
	v_pk_mul_f32 v[36:37], v[36:37], v[240:241]
	v_pk_mul_f32 v[46:47], v[46:47], v[234:235]
	v_pk_mul_f32 v[42:43], v[42:43], v[238:239]
	v_pk_mul_f32 v[38:39], v[38:39], v[242:243]
	v_pk_mul_f32 v[34:35], v[34:35], v[246:247]
	v_pk_mul_f32 v[32:33], v[32:33], v[244:245]
	v_pk_mul_f32 v[28:29], v[28:29], v[232:233]
	v_pk_mul_f32 v[24:25], v[24:25], v[236:237]
	v_pk_mul_f32 v[20:21], v[20:21], v[240:241]
	v_pk_mul_f32 v[30:31], v[30:31], v[234:235]
	v_pk_mul_f32 v[26:27], v[26:27], v[238:239]
	v_pk_mul_f32 v[22:23], v[22:23], v[242:243]
	v_pk_mul_f32 v[18:19], v[18:19], v[246:247]
	v_pk_mul_f32 v[16:17], v[16:17], v[244:245]
	v_pk_mul_f32 v[60:61], v[60:61], v[232:233]
	v_pk_mul_f32 v[56:57], v[56:57], v[236:237]
	v_pk_mul_f32 v[52:53], v[52:53], v[240:241]
	v_pk_mul_f32 v[62:63], v[62:63], v[234:235]
	v_pk_mul_f32 v[58:59], v[58:59], v[238:239]
	v_pk_mul_f32 v[54:55], v[54:55], v[242:243]
	v_pk_mul_f32 v[50:51], v[50:51], v[246:247]
	v_pk_mul_f32 v[48:49], v[48:49], v[244:245]
.LBB0_2016:
	ds_read_b128 v[64:67], v180 offset:32768
	ds_read_b128 v[68:71], v180 offset:40960
	ds_read_b128 v[222:225], v181 offset:32768
	ds_read_b128 v[226:229], v181 offset:40960
	ds_read_b128 v[230:233], v182 offset:32768
	ds_read_b128 v[234:237], v182 offset:40960
	ds_read_b128 v[238:241], v183 offset:32768
	ds_read_b128 v[242:245], v183 offset:40960
	v_exp_f32_e32 v164, v215
	v_add_f32_e32 v215, 0, v128
	s_waitcnt lgkmcnt(7)
	v_mfma_f32_32x32x16_bf16 v[80:95], v[64:67], v[124:127], 0
	v_add_f32_e32 v215, v198, v215
	v_add_f32_e32 v215, v129, v215
	v_add_f32_e32 v215, v163, v215
	v_add_f32_e32 v215, v130, v215
	v_add_f32_e32 v215, v162, v215
	v_add_f32_e32 v215, v131, v215
	v_add_f32_e32 v215, v161, v215
	s_waitcnt lgkmcnt(6)
	v_mfma_f32_32x32x16_bf16 v[64:79], v[68:71], v[124:127], 0
	v_add_f32_e32 v215, v132, v215
	v_add_f32_e32 v215, v139, v215
	v_add_f32_e32 v215, v133, v215
	v_add_f32_e32 v215, v138, v215
	v_add_f32_e32 v215, v134, v215
	v_exp_f32_e32 v165, v216
	v_add_f32_e32 v215, v137, v215
	s_waitcnt lgkmcnt(5)
	v_mfma_f32_32x32x16_bf16 v[80:95], v[222:225], v[120:123], v[80:95]
	v_exp_f32_e32 v217, v217
	v_add_f32_e32 v215, v135, v215
	v_exp_f32_e32 v218, v218
	v_add_f32_e32 v215, v136, v215
	v_exp_f32_e32 v219, v219
	v_add_f32_e32 v215, v164, v215
	v_exp_f32_e32 v208, v208
	s_waitcnt lgkmcnt(4)
	v_mfma_f32_32x32x16_bf16 v[64:79], v[226:229], v[120:123], v[64:79]
	ds_read_b128 v[222:225], v184 offset:32768
	ds_read_b128 v[226:229], v184 offset:40960
	v_add_f32_e32 v215, v165, v215
	v_exp_f32_e32 v209, v209
	v_add_f32_e32 v215, v217, v215
	v_exp_f32_e32 v210, v210
	v_add_f32_e32 v215, v218, v215
	v_exp_f32_e32 v211, v211
	s_waitcnt lgkmcnt(5)
	v_mfma_f32_32x32x16_bf16 v[80:95], v[230:233], v[116:119], v[80:95]
	v_add_f32_e32 v215, v219, v215
	v_exp_f32_e32 v212, v212
	v_add_f32_e32 v215, v208, v215
	v_exp_f32_e32 v213, v213
	v_add_f32_e32 v215, v209, v215
	v_exp_f32_e32 v214, v214
	v_add_f32_e32 v215, v210, v215
	s_waitcnt lgkmcnt(4)
	v_mfma_f32_32x32x16_bf16 v[64:79], v[234:237], v[116:119], v[64:79]
	ds_read_b128 v[230:233], v185 offset:32768
	ds_read_b128 v[234:237], v185 offset:40960
	v_exp_f32_e32 v207, v207
	v_add_f32_e32 v215, v211, v215
	v_exp_f32_e32 v220, v220
	v_add_f32_e32 v215, v212, v215
	v_exp_f32_e32 v221, v221
	v_add_f32_e32 v215, v213, v215
	s_waitcnt lgkmcnt(5)
	v_mfma_f32_32x32x16_bf16 v[80:95], v[238:241], v[112:115], v[80:95]
	v_exp_f32_e32 v205, v205
	v_add_f32_e32 v215, v214, v215
	v_add_f32_e32 v215, v207, v215
	v_add_f32_e32 v215, v220, v215
	v_add_f32_e32 v215, v221, v215
	v_add_f32_e32 v215, v205, v215
	v_mov_b32_e32 v216, v215
	s_waitcnt lgkmcnt(4)
	v_mfma_f32_32x32x16_bf16 v[64:79], v[242:245], v[112:115], v[64:79]
	ds_read_b128 v[238:241], v186 offset:32768
	ds_read_b128 v[242:245], v186 offset:40960
	v_permlane32_swap_b32_e32 v215, v216
	v_cvt_pk_bf16_f32 v128, v128, v198
	v_cvt_pk_bf16_f32 v129, v129, v163
	v_cvt_pk_bf16_f32 v130, v130, v162
	v_cvt_pk_bf16_f32 v131, v131, v161
	s_waitcnt lgkmcnt(5)
	v_mfma_f32_32x32x16_bf16 v[80:95], v[222:225], v[108:111], v[80:95]
	v_cvt_pk_bf16_f32 v132, v132, v139
	v_cvt_pk_bf16_f32 v133, v133, v138
	v_cvt_pk_bf16_f32 v134, v134, v137
	v_cvt_pk_bf16_f32 v135, v135, v136
	v_cvt_pk_bf16_f32 v136, v164, v165
	v_cvt_pk_bf16_f32 v137, v217, v218
	v_cvt_pk_bf16_f32 v138, v219, v208
	s_waitcnt lgkmcnt(4)
	v_mfma_f32_32x32x16_bf16 v[64:79], v[226:229], v[108:111], v[64:79]
	ds_read_b128 v[222:225], v187 offset:32768
	ds_read_b128 v[226:229], v187 offset:40960
	v_cvt_pk_bf16_f32 v139, v209, v210
	v_cvt_pk_bf16_f32 v208, v211, v212
	v_cvt_pk_bf16_f32 v209, v213, v214
	v_cvt_pk_bf16_f32 v210, v207, v220
	v_cvt_pk_bf16_f32 v211, v221, v205
	v_permlane32_swap_b32_e32 v128, v130
	s_waitcnt lgkmcnt(5)
	v_mfma_f32_32x32x16_bf16 v[80:95], v[230:233], v[104:107], v[80:95]
	v_permlane32_swap_b32_e32 v129, v131
	v_permlane32_swap_b32_e32 v132, v134
	v_permlane32_swap_b32_e32 v133, v135
	v_permlane32_swap_b32_e32 v136, v138
	s_waitcnt lgkmcnt(4)
	v_mfma_f32_32x32x16_bf16 v[64:79], v[234:237], v[104:107], v[64:79]
	ds_read_b128 v[230:233], v191
	ds_read_b128 v[234:237], v191 offset:4096
	ds_read_b128 v[246:249], v190
	v_permlane32_swap_b32_e32 v137, v139
	v_permlane32_swap_b32_e32 v208, v210
	v_permlane32_swap_b32_e32 v209, v211
	s_waitcnt lgkmcnt(6)
	v_mfma_f32_32x32x16_bf16 v[80:95], v[238:241], v[100:103], v[80:95]
	s_waitcnt lgkmcnt(5)
	v_mfma_f32_32x32x16_bf16 v[64:79], v[242:245], v[100:103], v[64:79]
	ds_read_b128 v[238:241], v192
	ds_read_b128 v[242:245], v192 offset:4096
	ds_read_b128 v[250:253], v190 offset:1024
	s_waitcnt lgkmcnt(7)
	v_mfma_f32_32x32x16_bf16 v[80:95], v[222:225], v[96:99], v[80:95]
	s_waitcnt lgkmcnt(6)
	v_mfma_f32_32x32x16_bf16 v[64:79], v[226:229], v[96:99], v[64:79]
	ds_read_b128 v[222:225], v193
	ds_read_b128 v[226:229], v193 offset:4096
	s_waitcnt lgkmcnt(5)
	v_mfma_f32_32x32x16_bf16 v[80:95], v[230:233], v[246:249], v[80:95]
	s_waitcnt lgkmcnt(5)
	v_mfma_f32_32x32x16_bf16 v[64:79], v[234:237], v[246:249], v[64:79]
	ds_read_b128 v[230:233], v194
	ds_read_b128 v[234:237], v194 offset:4096
	ds_read_b128 v[246:249], v190 offset:2048
	s_waitcnt lgkmcnt(5)
	v_mfma_f32_32x32x16_bf16 v[80:95], v[238:241], v[250:253], v[80:95]
	s_waitcnt lgkmcnt(5)
	v_mfma_f32_32x32x16_bf16 v[64:79], v[242:245], v[250:253], v[64:79]
	ds_read_b128 v[250:253], v190 offset:3072
	s_waitcnt lgkmcnt(1)
	v_mfma_f32_32x32x16_bf16 v[80:95], v[222:225], v[246:249], v[80:95]
	s_waitcnt lgkmcnt(1)
	v_mfma_f32_32x32x16_bf16 v[64:79], v[226:229], v[246:249], v[64:79]
	s_waitcnt lgkmcnt(0)
	v_mfma_f32_32x32x16_bf16 v[80:95], v[230:233], v[250:253], v[80:95]
	s_waitcnt lgkmcnt(0)
	v_mfma_f32_32x32x16_bf16 v[64:79], v[234:237], v[250:253], v[64:79]
	ds_read_b64_tr_b16 v[238:239], v174 offset:0
	ds_read_b64_tr_b16 v[240:241], v174 offset:0x800
	ds_read_b64_tr_b16 v[242:243], v174 offset:0x1000
	ds_read_b64_tr_b16 v[244:245], v174 offset:0x1800
	ds_read_b64_tr_b16 v[246:247], v174 offset:0x2000
	ds_read_b64_tr_b16 v[248:249], v174 offset:0x2800
	ds_read_b64_tr_b16 v[250:251], v174 offset:0x3000
	ds_read_b64_tr_b16 v[252:253], v174 offset:0x3800
	s_nop 3
	v_max_f32_e32 v161, v81, v81
	v_max_f32_e32 v162, v80, v80
	v_max_f32_e32 v161, v162, v161
	v_max3_f32 v161, v161, v82, v83
	v_max3_f32 v161, v161, v84, v85
	v_max3_f32 v161, v161, v86, v87
	v_max3_f32 v161, v161, v88, v89
	v_max3_f32 v161, v161, v90, v91
	v_max3_f32 v161, v161, v92, v93
	v_max3_f32 v161, v161, v94, v95
	s_waitcnt lgkmcnt(0)
	v_mfma_f32_32x32x16_bf16 v[0:15], v[128:131], v[238:241], v[0:15]
	ds_read_b64_tr_b16 v[238:239], v174 offset:0x200
	ds_read_b64_tr_b16 v[240:241], v174 offset:0xa00
	v_max3_f32 v161, v161, v64, v65
	v_max3_f32 v161, v161, v66, v67
	v_max3_f32 v161, v161, v68, v69
	v_mfma_f32_32x32x16_bf16 v[0:15], v[132:135], v[242:245], v[0:15]
	ds_read_b64_tr_b16 v[242:243], v174 offset:0x1200
	ds_read_b64_tr_b16 v[244:245], v174 offset:0x1a00
	v_max3_f32 v161, v161, v70, v71
	v_max3_f32 v161, v161, v72, v73
	v_max3_f32 v161, v161, v74, v75
	v_mfma_f32_32x32x16_bf16 v[0:15], v[136:139], v[246:249], v[0:15]
	ds_read_b64_tr_b16 v[246:247], v174 offset:0x2200
	ds_read_b64_tr_b16 v[248:249], v174 offset:0x2a00
	ds_read_b64_tr_b16 v[162:163], v174 offset:0x3200
	ds_read_b64_tr_b16 v[164:165], v174 offset:0x3a00
	v_max3_f32 v161, v161, v76, v77
	v_max3_f32 v161, v161, v78, v79
	v_mov_b32_e32 v198, v161
	v_mfma_f32_32x32x16_bf16 v[0:15], v[208:211], v[250:253], v[0:15]
	v_max_f32_e32 v205, v160, v160
	v_permlane32_swap_b32_e32 v161, v198
	v_max_f32_e32 v198, v198, v198
	v_max_f32_e32 v161, v161, v161
	v_max_f32_e32 v161, v161, v198
	s_waitcnt lgkmcnt(0)
	v_mfma_f32_32x32x16_bf16 v[32:47], v[128:131], v[238:241], v[32:47]
	ds_read_b64_tr_b16 v[238:239], v174 offset:0x400
	ds_read_b64_tr_b16 v[240:241], v174 offset:0xc00
	v_sub_f32_e32 v198, v161, v160
	v_max_f32_e32 v161, v205, v161
	v_sub_f32_e32 v205, v160, v161
	v_mul_f32_e32 v205, 0x3dd53b94, v205
	v_exp_f32_e32 v205, v205
	v_mfma_f32_32x32x16_bf16 v[32:47], v[132:135], v[242:245], v[32:47]
	ds_read_b64_tr_b16 v[242:243], v174 offset:0x1400
	ds_read_b64_tr_b16 v[244:245], v174 offset:0x1c00
	v_cmp_ge_f32_e32 vcc, s46, v198
	s_cmp_eq_u64 vcc, exec
	s_cselect_b64 s[6:7], -1, 0
	v_cndmask_b32_e64 v205, v205, 1.0, s[6:7]
	v_cndmask_b32_e64 v198, v161, v160, s[6:7]
	v_mul_f32_e32 v236, 0xbdd53b94, v198
	v_mov_b32_e32 v237, v236
	v_cmp_gt_f32_e32 vcc, 1.0, v205
	v_mfma_f32_32x32x16_bf16 v[32:47], v[136:139], v[246:249], v[32:47]
	ds_read_b64_tr_b16 v[246:247], v174 offset:0x2400
	ds_read_b64_tr_b16 v[248:249], v174 offset:0x2c00
	ds_read_b64_tr_b16 v[250:251], v174 offset:0x3400
	ds_read_b64_tr_b16 v[252:253], v174 offset:0x3c00
	v_fmamk_f32 v80, v80, 0x3dd53b94, v236
	v_fmamk_f32 v81, v81, 0x3dd53b94, v236
	v_fmamk_f32 v82, v82, 0x3dd53b94, v236
	v_fmamk_f32 v83, v83, 0x3dd53b94, v236
	v_mfma_f32_32x32x16_bf16 v[32:47], v[208:211], v[162:165], v[32:47]
	v_fmamk_f32 v84, v84, 0x3dd53b94, v236
	v_fmamk_f32 v85, v85, 0x3dd53b94, v236
	v_fmamk_f32 v86, v86, 0x3dd53b94, v236
	v_fmamk_f32 v87, v87, 0x3dd53b94, v236
	s_waitcnt lgkmcnt(0)
	v_mfma_f32_32x32x16_bf16 v[16:31], v[128:131], v[238:241], v[16:31]
	ds_read_b64_tr_b16 v[162:163], v174 offset:0x600
	ds_read_b64_tr_b16 v[164:165], v174 offset:0xe00
	ds_read_b64_tr_b16 v[238:239], v174 offset:0x1600
	ds_read_b64_tr_b16 v[240:241], v174 offset:0x1e00
	v_fmamk_f32 v88, v88, 0x3dd53b94, v236
	v_fmamk_f32 v89, v89, 0x3dd53b94, v236
	v_fmamk_f32 v90, v90, 0x3dd53b94, v236
	v_fmamk_f32 v91, v91, 0x3dd53b94, v236
	v_mfma_f32_32x32x16_bf16 v[16:31], v[132:135], v[242:245], v[16:31]
	ds_read_b64_tr_b16 v[242:243], v174 offset:0x2600
	ds_read_b64_tr_b16 v[244:245], v174 offset:0x2e00
	v_fmamk_f32 v92, v92, 0x3dd53b94, v236
	v_fmamk_f32 v93, v93, 0x3dd53b94, v236
	v_fmamk_f32 v94, v94, 0x3dd53b94, v236
	v_fmamk_f32 v95, v95, 0x3dd53b94, v236
	v_mfma_f32_32x32x16_bf16 v[16:31], v[136:139], v[246:249], v[16:31]
	ds_read_b64_tr_b16 v[246:247], v174 offset:0x3600
	ds_read_b64_tr_b16 v[248:249], v174 offset:0x3e00
	v_exp_f32_e32 v222, v80
	v_exp_f32_e32 v224, v81
	v_exp_f32_e32 v220, v82
	v_mfma_f32_32x32x16_bf16 v[16:31], v[208:211], v[250:253], v[16:31]
	v_exp_f32_e32 v223, v83
	v_exp_f32_e32 v219, v84
	v_exp_f32_e32 v221, v85
	s_waitcnt vmcnt(0) lgkmcnt(0)
	s_barrier
	v_mfma_f32_32x32x16_bf16 v[48:63], v[128:131], v[162:165], v[48:63]
	s_addk_i32 s13, 0x80
	s_addk_i32 s14, 0x80
	s_sub_i32 s80, s14, 64
	s_mul_i32 s81, s80, 0xc00
	s_add_i32 s85, s82, 0x8000
	s_mov_b32 m0, s85
	s_add_i32 s85, s82, 0x10000
	buffer_load_dwordx4 v154, s[72:75], s81 offen lds
	v_exp_f32_e32 v217, v86
	v_exp_f32_e32 v218, v87
	v_exp_f32_e32 v212, v88
	v_pk_fma_f32 v[130:131], v[70:71], s[26:27], v[236:237] op_sel_hi:[1,0,0]
	v_pk_fma_f32 v[128:129], v[72:73], s[26:27], v[236:237] op_sel_hi:[1,0,0]
	v_mfma_f32_32x32x16_bf16 v[48:63], v[132:135], v[238:241], v[48:63]
	s_mov_b32 m0, s85
	s_add_i32 s85, s82, 0xa000
	buffer_load_dwordx4 v155, s[72:75], s81 offen lds
	v_exp_f32_e32 v214, v89
	v_exp_f32_e32 v213, v91
	v_exp_f32_e32 v207, v94
	v_pk_fma_f32 v[132:133], v[68:69], s[26:27], v[236:237] op_sel_hi:[1,0,0]
	v_pk_fma_f32 v[134:135], v[78:79], s[26:27], v[236:237] op_sel_hi:[1,0,0]
	v_mfma_f32_32x32x16_bf16 v[48:63], v[136:139], v[242:245], v[48:63]
	s_mov_b32 m0, s85
	s_add_i32 s81, s81, 0x18000
	buffer_load_dwordx4 v154, s[72:75], s81 offen lds
	v_pk_fma_f32 v[138:139], v[64:65], s[26:27], v[236:237] op_sel_hi:[1,0,0]
	v_pk_fma_f32 v[136:137], v[66:67], s[26:27], v[236:237] op_sel_hi:[1,0,0]
	v_pk_fma_f32 v[162:163], v[74:75], s[26:27], v[236:237] op_sel_hi:[1,0,0]
	v_pk_fma_f32 v[160:161], v[76:77], s[26:27], v[236:237] op_sel_hi:[1,0,0]
	v_mfma_f32_32x32x16_bf16 v[48:63], v[208:211], v[246:249], v[48:63]
	s_lshl_b32 s81, s83, 11
	s_add_i32 s85, s82, 0x4000
	s_mov_b32 m0, s85
	s_add_i32 s85, s82, 0x6000
	buffer_load_dwordx4 v158, s[76:79], s81 offen lds
	s_mov_b32 m0, s85
	s_add_i32 s81, s81, 0x10000
	buffer_load_dwordx4 v158, s[76:79], s81 offen lds
	s_mov_b32 s84, s80
	v_exp_f32_e32 v211, v90
	v_exp_f32_e32 v208, v92
	v_exp_f32_e32 v210, v93
	v_exp_f32_e32 v209, v95
	v_add_f32_e32 v64, v203, v204
	v_fmac_f32_e32 v64, v197, v140
	v_add_f32_e32 v140, v215, v216
	v_fmac_f32_e32 v140, v64, v206
	s_cbranch_vccz .LBB0_2020
	s_and_saveexec_b64 s[10:11], s[4:5]
	ds_write_b32 v189, v205 offset:128
	s_or_b64 exec, exec, s[10:11]
	s_waitcnt lgkmcnt(0)
	v_add_u32_e32 v164, s12, v169
	ds_read_b128 v[238:241], v164 offset:224
	ds_read_b128 v[242:245], v164 offset:192
	ds_read_b128 v[246:249], v164 offset:160
	ds_read_b128 v[250:253], v164 offset:128
	s_waitcnt lgkmcnt(3)
	v_pk_mul_f32 v[12:13], v[12:13], v[238:239]
	s_waitcnt lgkmcnt(2)
	v_pk_mul_f32 v[8:9], v[8:9], v[242:243]
	s_waitcnt lgkmcnt(1)
	v_pk_mul_f32 v[4:5], v[4:5], v[246:247]
	v_pk_mul_f32 v[14:15], v[14:15], v[240:241]
	v_pk_mul_f32 v[10:11], v[10:11], v[244:245]
	v_pk_mul_f32 v[6:7], v[6:7], v[248:249]
	s_waitcnt lgkmcnt(0)
	v_pk_mul_f32 v[2:3], v[2:3], v[252:253]
	v_pk_mul_f32 v[0:1], v[0:1], v[250:251]
	v_pk_mul_f32 v[44:45], v[44:45], v[238:239]
	v_pk_mul_f32 v[40:41], v[40:41], v[242:243]
	v_pk_mul_f32 v[36:37], v[36:37], v[246:247]
	v_pk_mul_f32 v[46:47], v[46:47], v[240:241]
	v_pk_mul_f32 v[42:43], v[42:43], v[244:245]
	v_pk_mul_f32 v[38:39], v[38:39], v[248:249]
	v_pk_mul_f32 v[34:35], v[34:35], v[252:253]
	v_pk_mul_f32 v[32:33], v[32:33], v[250:251]
	v_pk_mul_f32 v[28:29], v[28:29], v[238:239]
	v_pk_mul_f32 v[24:25], v[24:25], v[242:243]
	v_pk_mul_f32 v[20:21], v[20:21], v[246:247]
	v_pk_mul_f32 v[30:31], v[30:31], v[240:241]
	v_pk_mul_f32 v[26:27], v[26:27], v[244:245]
	v_pk_mul_f32 v[22:23], v[22:23], v[248:249]
	v_pk_mul_f32 v[18:19], v[18:19], v[252:253]
	v_pk_mul_f32 v[16:17], v[16:17], v[250:251]
	v_pk_mul_f32 v[60:61], v[60:61], v[238:239]
	v_pk_mul_f32 v[56:57], v[56:57], v[242:243]
	v_pk_mul_f32 v[52:53], v[52:53], v[246:247]
	v_pk_mul_f32 v[62:63], v[62:63], v[240:241]
	v_pk_mul_f32 v[58:59], v[58:59], v[244:245]
	v_pk_mul_f32 v[54:55], v[54:55], v[248:249]
	v_pk_mul_f32 v[50:51], v[50:51], v[252:253]
	v_pk_mul_f32 v[48:49], v[48:49], v[250:251]
.LBB0_2020:
	s_cmp_gt_u32 s8, 64
	s_cbranch_scc1 .LBB0_2022
	v_mov_b32_e32 v197, v205
	s_branch .LBB0_2012
.LBB0_2022:
	ds_read_b128 v[64:67], v180 offset:49152
	ds_read_b128 v[68:71], v180 offset:57344
	v_exp_f32_e32 v138, v138
	v_exp_f32_e32 v139, v139
	v_exp_f32_e32 v136, v136
	s_waitcnt lgkmcnt(1)
	v_mfma_f32_32x32x16_bf16 v[80:95], v[64:67], v[124:127], 0
	v_exp_f32_e32 v137, v137
	v_exp_f32_e32 v132, v132
	v_exp_f32_e32 v128, v128
	v_exp_f32_e32 v129, v129
	s_waitcnt lgkmcnt(0)
	v_mfma_f32_32x32x16_bf16 v[64:79], v[68:71], v[124:127], 0
	ds_read_b128 v[124:127], v181 offset:49152
	ds_read_b128 v[154:157], v181 offset:57344
	s_waitcnt lgkmcnt(1)
	v_mfma_f32_32x32x16_bf16 v[80:95], v[124:127], v[120:123], v[80:95]
	s_waitcnt lgkmcnt(0)
	v_mfma_f32_32x32x16_bf16 v[64:79], v[154:157], v[120:123], v[64:79]
	ds_read_b128 v[120:123], v182 offset:49152
	ds_read_b128 v[124:127], v182 offset:57344
	s_waitcnt lgkmcnt(1)
	v_mfma_f32_32x32x16_bf16 v[80:95], v[120:123], v[116:119], v[80:95]
	s_waitcnt lgkmcnt(0)
	v_mfma_f32_32x32x16_bf16 v[64:79], v[124:127], v[116:119], v[64:79]
	ds_read_b128 v[116:119], v183 offset:49152
	ds_read_b128 v[120:123], v183 offset:57344
	s_waitcnt lgkmcnt(1)
	v_mfma_f32_32x32x16_bf16 v[80:95], v[116:119], v[112:115], v[80:95]
	s_waitcnt lgkmcnt(0)
	v_mfma_f32_32x32x16_bf16 v[64:79], v[120:123], v[112:115], v[64:79]
	ds_read_b128 v[112:115], v184 offset:49152
	ds_read_b128 v[116:119], v184 offset:57344
	s_waitcnt lgkmcnt(1)
	v_mfma_f32_32x32x16_bf16 v[80:95], v[112:115], v[108:111], v[80:95]
	ds_read_b128 v[112:115], v185 offset:49152
	s_waitcnt lgkmcnt(1)
	v_mfma_f32_32x32x16_bf16 v[64:79], v[116:119], v[108:111], v[64:79]
	ds_read_b128 v[108:111], v185 offset:57344
	ds_read_b128 v[116:119], v186 offset:49152
	ds_read_b128 v[120:123], v186 offset:57344
	ds_read_b128 v[124:127], v187 offset:49152
	ds_read_b128 v[154:157], v187 offset:57344
	ds_read_b128 v[192:195], v199
	ds_read_b128 v[226:229], v199 offset:4096
	s_waitcnt lgkmcnt(7)
	v_mfma_f32_32x32x16_bf16 v[80:95], v[112:115], v[104:107], v[80:95]
	ds_read_b128 v[112:115], v200
	ds_read_b128 v[230:233], v200 offset:4096
	ds_read_b128 v[234:237], v190
	ds_read_b128 v[238:241], v190 offset:1024
	ds_read_b128 v[242:245], v201
	ds_read_b128 v[246:249], v201 offset:4096
	ds_read_b128 v[250:253], v202
	ds_read_b128 v[200:203], v202 offset:4096
	s_waitcnt lgkmcnt(14)
	v_mfma_f32_32x32x16_bf16 v[64:79], v[108:111], v[104:107], v[64:79]
	ds_read_b128 v[104:107], v190 offset:2048
	ds_read_b128 v[108:111], v190 offset:3072
	s_waitcnt lgkmcnt(14)
	v_mfma_f32_32x32x16_bf16 v[80:95], v[116:119], v[100:103], v[80:95]
	v_exp_f32_e32 v118, v133
	v_exp_f32_e32 v119, v130
	v_exp_f32_e32 v130, v131
	v_exp_f32_e32 v131, v162
	v_exp_f32_e32 v133, v163
	v_cvt_pk_bf16_f32 v116, v138, v139
	v_cvt_pk_bf16_f32 v117, v136, v137
	v_mfma_f32_32x32x16_bf16 v[64:79], v[120:123], v[100:103], v[64:79]
	v_add_f32_e32 v100, 0, v222
	v_add_f32_e32 v100, v224, v100
	v_add_f32_e32 v100, v220, v100
	v_add_f32_e32 v100, v223, v100
	v_add_f32_e32 v100, v219, v100
	v_add_f32_e32 v100, v221, v100
	v_add_f32_e32 v100, v217, v100
	s_waitcnt lgkmcnt(13)
	v_mfma_f32_32x32x16_bf16 v[80:95], v[124:127], v[96:99], v[80:95]
	v_add_f32_e32 v100, v218, v100
	v_add_f32_e32 v100, v212, v100
	v_add_f32_e32 v100, v214, v100
	v_exp_f32_e32 v120, v160
	v_exp_f32_e32 v121, v161
	v_exp_f32_e32 v122, v134
	v_exp_f32_e32 v123, v135
	s_waitcnt lgkmcnt(12)
	v_mfma_f32_32x32x16_bf16 v[64:79], v[154:157], v[96:99], v[64:79]
	v_add_f32_e32 v96, v211, v100
	v_add_f32_e32 v96, v213, v96
	v_add_f32_e32 v96, v208, v96
	v_add_f32_e32 v96, v210, v96
	v_add_f32_e32 v96, v207, v96
	v_add_f32_e32 v96, v209, v96
	v_add_f32_e32 v96, v138, v96
	s_waitcnt lgkmcnt(7)
	v_mfma_f32_32x32x16_bf16 v[80:95], v[192:195], v[234:237], v[80:95]
	v_add_f32_e32 v96, v139, v96
	v_add_f32_e32 v96, v136, v96
	v_add_f32_e32 v96, v137, v96
	v_add_f32_e32 v96, v132, v96
	v_add_f32_e32 v96, v118, v96
	v_add_f32_e32 v96, v119, v96
	v_add_f32_e32 v96, v130, v96
	v_mfma_f32_32x32x16_bf16 v[64:79], v[226:229], v[234:237], v[64:79]
	v_add_f32_e32 v96, v128, v96
	v_add_f32_e32 v96, v129, v96
	v_add_f32_e32 v96, v131, v96
	v_add_f32_e32 v96, v133, v96
	v_add_f32_e32 v96, v120, v96
	v_add_f32_e32 v96, v121, v96
	v_add_f32_e32 v96, v122, v96
	s_waitcnt lgkmcnt(6)
	v_mfma_f32_32x32x16_bf16 v[80:95], v[112:115], v[238:241], v[80:95]
	v_add_f32_e32 v96, v123, v96
	v_mov_b32_e32 v97, v96
	s_nop 1
	v_permlane32_swap_b32_e32 v96, v97
	v_cvt_pk_bf16_f32 v100, v222, v224
	v_cvt_pk_bf16_f32 v101, v220, v223
	v_cvt_pk_bf16_f32 v102, v219, v221
	v_mfma_f32_32x32x16_bf16 v[64:79], v[230:233], v[238:241], v[64:79]
	v_cvt_pk_bf16_f32 v103, v217, v218
	v_cvt_pk_bf16_f32 v112, v212, v214
	v_cvt_pk_bf16_f32 v113, v211, v213
	v_cvt_pk_bf16_f32 v114, v208, v210
	v_cvt_pk_bf16_f32 v115, v207, v209
	v_cvt_pk_bf16_f32 v118, v132, v118
	v_cvt_pk_bf16_f32 v119, v119, v130
	s_waitcnt lgkmcnt(1)
	v_mfma_f32_32x32x16_bf16 v[80:95], v[242:245], v[104:107], v[80:95]
	v_permlane32_swap_b32_e32 v100, v102
	v_permlane32_swap_b32_e32 v101, v103
	v_permlane32_swap_b32_e32 v112, v114
	v_permlane32_swap_b32_e32 v113, v115
	v_mfma_f32_32x32x16_bf16 v[64:79], v[246:249], v[104:107], v[64:79]
	v_cvt_pk_bf16_f32 v104, v128, v129
	v_cvt_pk_bf16_f32 v105, v131, v133
	v_cvt_pk_bf16_f32 v106, v120, v121
	v_cvt_pk_bf16_f32 v107, v122, v123
	v_permlane32_swap_b32_e32 v116, v118
	v_permlane32_swap_b32_e32 v117, v119
	s_waitcnt lgkmcnt(0)
	v_mfma_f32_32x32x16_bf16 v[80:95], v[250:253], v[108:111], v[80:95]
	v_permlane32_swap_b32_e32 v104, v106
	v_permlane32_swap_b32_e32 v105, v107
	v_mfma_f32_32x32x16_bf16 v[64:79], v[200:203], v[108:111], v[64:79]
	ds_read_b64_tr_b16 v[108:109], v167 offset:0
	ds_read_b64_tr_b16 v[110:111], v167 offset:0x800
	ds_read_b64_tr_b16 v[120:121], v167 offset:0x1000
	ds_read_b64_tr_b16 v[122:123], v167 offset:0x1800
	ds_read_b64_tr_b16 v[124:125], v167 offset:0x2000
	ds_read_b64_tr_b16 v[126:127], v167 offset:0x2800
	ds_read_b64_tr_b16 v[128:129], v167 offset:0x3000
	ds_read_b64_tr_b16 v[130:131], v167 offset:0x3800
	s_nop 8
	v_max_f32_e32 v98, v81, v81
	v_max_f32_e32 v99, v80, v80
	v_max_f32_e32 v98, v99, v98
	v_max3_f32 v98, v98, v82, v83
	v_max3_f32 v98, v98, v84, v85
	v_max3_f32 v98, v98, v86, v87
	v_max3_f32 v98, v98, v88, v89
	v_max3_f32 v98, v98, v90, v91
	v_max3_f32 v98, v98, v92, v93
	v_max3_f32 v98, v98, v94, v95
	s_waitcnt lgkmcnt(0)
	v_mfma_f32_32x32x16_bf16 v[0:15], v[100:103], v[108:111], v[0:15]
	ds_read_b64_tr_b16 v[108:109], v167 offset:0x200
	ds_read_b64_tr_b16 v[110:111], v167 offset:0xa00
	v_mfma_f32_32x32x16_bf16 v[0:15], v[112:115], v[120:123], v[0:15]
	ds_read_b64_tr_b16 v[120:121], v167 offset:0x1200
	ds_read_b64_tr_b16 v[122:123], v167 offset:0x1a00
	v_mfma_f32_32x32x16_bf16 v[0:15], v[116:119], v[124:127], v[0:15]
	ds_read_b64_tr_b16 v[124:125], v167 offset:0x2200
	ds_read_b64_tr_b16 v[126:127], v167 offset:0x2a00
	ds_read_b64_tr_b16 v[132:133], v167 offset:0x3200
	ds_read_b64_tr_b16 v[134:135], v167 offset:0x3a00
	v_mfma_f32_32x32x16_bf16 v[0:15], v[104:107], v[128:131], v[0:15]
	v_max3_f32 v98, v98, v64, v65
	v_max3_f32 v98, v98, v66, v67
	v_max3_f32 v98, v98, v68, v69
	v_max3_f32 v98, v98, v70, v71
	v_max3_f32 v98, v98, v72, v73
	v_max3_f32 v98, v98, v74, v75
	v_max3_f32 v98, v98, v76, v77
	v_max3_f32 v98, v98, v78, v79
	v_mov_b32_e32 v99, v98
	s_nop 1
	v_permlane32_swap_b32_e32 v98, v99
	v_max_f32_e32 v99, v99, v99
	v_max_f32_e32 v98, v98, v98
	v_max_f32_e32 v98, v98, v99
	v_max_f32_e32 v99, v198, v198
	v_max_f32_e32 v99, v99, v98
	v_sub_f32_e32 v128, v98, v198
	v_sub_f32_e32 v98, v198, v99
	v_mul_f32_e32 v98, 0x3dd53b94, v98
	v_exp_f32_e32 v98, v98
	v_cmp_ge_f32_e32 vcc, s46, v128
	s_cmp_eq_u64 vcc, exec
	s_cselect_b64 s[6:7], -1, 0
	v_cndmask_b32_e64 v98, v98, 1.0, s[6:7]
	s_waitcnt lgkmcnt(0)
	v_mfma_f32_32x32x16_bf16 v[32:47], v[100:103], v[108:111], v[32:47]
	ds_read_b64_tr_b16 v[108:109], v167 offset:0x400
	ds_read_b64_tr_b16 v[110:111], v167 offset:0xc00
	v_mfma_f32_32x32x16_bf16 v[32:47], v[112:115], v[120:123], v[32:47]
	ds_read_b64_tr_b16 v[120:121], v167 offset:0x1400
	ds_read_b64_tr_b16 v[122:123], v167 offset:0x1c00
	v_mfma_f32_32x32x16_bf16 v[32:47], v[116:119], v[124:127], v[32:47]
	ds_read_b64_tr_b16 v[124:125], v167 offset:0x2400
	ds_read_b64_tr_b16 v[126:127], v167 offset:0x2c00
	ds_read_b64_tr_b16 v[128:129], v167 offset:0x3400
	ds_read_b64_tr_b16 v[130:131], v167 offset:0x3c00
	v_mfma_f32_32x32x16_bf16 v[32:47], v[104:107], v[132:135], v[32:47]
	s_waitcnt lgkmcnt(0)
	v_mfma_f32_32x32x16_bf16 v[16:31], v[100:103], v[108:111], v[16:31]
	ds_read_b64_tr_b16 v[108:109], v167 offset:0x600
	ds_read_b64_tr_b16 v[110:111], v167 offset:0xe00
	v_mfma_f32_32x32x16_bf16 v[16:31], v[112:115], v[120:123], v[16:31]
	ds_read_b64_tr_b16 v[120:121], v167 offset:0x1600
	ds_read_b64_tr_b16 v[122:123], v167 offset:0x1e00
	v_mfma_f32_32x32x16_bf16 v[16:31], v[116:119], v[124:127], v[16:31]
	ds_read_b64_tr_b16 v[124:125], v167 offset:0x2600
	ds_read_b64_tr_b16 v[126:127], v167 offset:0x2e00
	ds_read_b64_tr_b16 v[132:133], v167 offset:0x3600
	ds_read_b64_tr_b16 v[134:135], v167 offset:0x3e00
	v_mfma_f32_32x32x16_bf16 v[16:31], v[104:107], v[128:131], v[16:31]
	s_waitcnt lgkmcnt(0)
	v_mfma_f32_32x32x16_bf16 v[48:63], v[100:103], v[108:111], v[48:63]
	v_cmp_gt_f32_e32 vcc, 1.0, v98
	s_waitcnt vmcnt(0)
	s_barrier
	v_mfma_f32_32x32x16_bf16 v[48:63], v[112:115], v[120:123], v[48:63]
	v_mfma_f32_32x32x16_bf16 v[48:63], v[116:119], v[124:127], v[48:63]
	v_mfma_f32_32x32x16_bf16 v[48:63], v[104:107], v[132:135], v[48:63]
	s_cbranch_vccz .LBB0_2026
	s_and_saveexec_b64 s[10:11], s[4:5]
	ds_write_b32 v189, v98 offset:128
	s_or_b64 exec, exec, s[10:11]
	s_waitcnt lgkmcnt(0)
	v_add_u32_e32 v112, s12, v169
	ds_read_b128 v[100:103], v112 offset:224
	ds_read_b128 v[104:107], v112 offset:192
	ds_read_b128 v[108:111], v112 offset:160
	ds_read_b128 v[112:115], v112 offset:128
	s_waitcnt lgkmcnt(3)
	v_pk_mul_f32 v[12:13], v[12:13], v[100:101]
	s_waitcnt lgkmcnt(2)
	v_pk_mul_f32 v[8:9], v[8:9], v[104:105]
	s_waitcnt lgkmcnt(1)
	v_pk_mul_f32 v[4:5], v[4:5], v[108:109]
	v_pk_mul_f32 v[14:15], v[14:15], v[102:103]
	v_pk_mul_f32 v[10:11], v[10:11], v[106:107]
	v_pk_mul_f32 v[6:7], v[6:7], v[110:111]
	s_waitcnt lgkmcnt(0)
	v_pk_mul_f32 v[2:3], v[2:3], v[114:115]
	v_pk_mul_f32 v[0:1], v[0:1], v[112:113]
	v_pk_mul_f32 v[44:45], v[44:45], v[100:101]
	v_pk_mul_f32 v[40:41], v[40:41], v[104:105]
	v_pk_mul_f32 v[36:37], v[36:37], v[108:109]
	v_pk_mul_f32 v[46:47], v[46:47], v[102:103]
	v_pk_mul_f32 v[42:43], v[42:43], v[106:107]
	v_pk_mul_f32 v[38:39], v[38:39], v[110:111]
	v_pk_mul_f32 v[34:35], v[34:35], v[114:115]
	v_pk_mul_f32 v[32:33], v[32:33], v[112:113]
	v_pk_mul_f32 v[28:29], v[28:29], v[100:101]
	v_pk_mul_f32 v[24:25], v[24:25], v[104:105]
	v_pk_mul_f32 v[20:21], v[20:21], v[108:109]
	v_pk_mul_f32 v[30:31], v[30:31], v[102:103]
	v_pk_mul_f32 v[26:27], v[26:27], v[106:107]
	v_pk_mul_f32 v[22:23], v[22:23], v[110:111]
	v_pk_mul_f32 v[18:19], v[18:19], v[114:115]
	v_pk_mul_f32 v[16:17], v[16:17], v[112:113]
	v_pk_mul_f32 v[60:61], v[60:61], v[100:101]
	v_pk_mul_f32 v[56:57], v[56:57], v[104:105]
	v_pk_mul_f32 v[52:53], v[52:53], v[108:109]
	v_pk_mul_f32 v[62:63], v[62:63], v[102:103]
	v_pk_mul_f32 v[58:59], v[58:59], v[106:107]
	v_pk_mul_f32 v[54:55], v[54:55], v[110:111]
	v_pk_mul_f32 v[50:51], v[50:51], v[114:115]
	v_pk_mul_f32 v[48:49], v[48:49], v[112:113]
